# mLSTM chunk-local units: gate values of all four heads and the two gate biases preloaded once per chunk by wave 0, the per-head vector step reads registers
# baseline (speedup 1.0000x reference)
; #define LAS __attribute__((address_space(3)))
; DI void ssd_vectors(Frame& F, int l, int t0, int g, LAS float* DT, LAS float* AC, LAS float* RED) {
;     (void)RED;
;     if (F.wave < 2) {
;         const int r2 = F.wave, head = 2 * g + r2, s0 = 2 * F.lane; const float* gp = (const float*)(F.ws + WS_GATES) + (size_t)(t0 + s0) * 16 + 4 + head;
;         const float db = inp(F, I_DTB)[l * 4 + head], na = -__expf(inp(F, I_ALOG)[l * 4 + head]);
; DI void ssd_local_unit(Frame& F, int l, int ch, int g) {
;     ...
;     const int t0 = ch * CHUNK, cpos = ch & (CPB - 1);
;     const bf16* proj = (const bf16*)(F.ws + WS_PROJ); bf16* xbcc = (bf16*)(F.ws + WS_XBCC);
;     const float* cw = inp(F, I_CONVW) + (size_t)l * 4 * XC; const float* cb = inp(F, I_CONVB) + (size_t)l * XC;
;     const int s = F.tid >> 2, cg = F.tid & 3;
;     float okm[4]; int spc[4];
; #pragma unroll
;     for (int j = 0; j < 4; ++j) { const int sp = s - 3 + j; const bool ok = cpos * CHUNK + sp >= 0; okm[j] = ok ? 1.f : 0.f; spc[j] = ok ? sp : s; }
;     auto load_part = [&](const int part, v4u (&raw)[4][4]) {
; #pragma unroll
;         for (int cc = 0; cc < 4; ++cc)
; #pragma unroll
;             for (int j = 0; j < 4; ++j) raw[cc][j] = *(const v4u*)(proj + (size_t)(t0 + spc[j]) * PP + O_XBC + part * 256 + g * 128 + cg * 32 + cc * 8); };
.LBB0_836:
	s_mov_b64 s[0:1], 0
	v_readfirstlane_b32 s38, v132
	s_ashr_i32 s37, s38, 6
	s_mov_b32 s35, 0
	s_add_u32 s20, s20, s0
	s_addc_u32 s21, s21, s1
	s_add_i32 s19, s17, s35
	v_ashrrev_i32_e32 v1, 2, v132
	s_add_i32 s41, s19, 0x19800
	v_add_u32_e32 v0, -3, v1
	v_add_u32_e32 v2, -2, v1
	s_add_u32 s24, s20, 0xb100000
	v_cmp_lt_i32_e32 vcc, s30, v0
	v_cmp_lt_i32_e64 s[2:3], s30, v2
	s_addc_u32 s25, s21, 0
	v_cndmask_b32_e32 v0, v1, v0, vcc
	s_waitcnt vmcnt(0)
	s_cmp_gt_u32 s38, 63
	s_cbranch_scc1 .Lmy_gpre_skip
	s_cmp_lg_u32 s34, 0
	s_cbranch_scc1 .Lmy_gpre_skip
	s_add_i32 s88, s19, 0x20868
	v_mov_b32_e32 v237, s88
	ds_read2_b32 v[246:247], v237 offset1:1
	ds_read2_b32 v[248:249], v237 offset0:2 offset1:3
	s_lshl_b32 s99, s14, 2
	v_and_b32_e32 v223, 63, v132
	v_lshl_or_b32 v223, v223, 1, s29
	v_lshlrev_b32_e32 v223, 6, v223
	s_add_u32 s74, s20, 0x500000
	s_addc_u32 s75, s21, 0
	global_load_dwordx4 v[218:221], v223, s[74:75] offset:32
	global_load_dwordx4 v[224:227], v223, s[74:75] offset:48
	global_load_dwordx4 v[238:241], v223, s[74:75] offset:96
	global_load_dwordx4 v[242:245], v223, s[74:75] offset:112
	s_waitcnt lgkmcnt(0)
	v_readfirstlane_b32 s88, v246
	v_readfirstlane_b32 s89, v247
	v_readfirstlane_b32 s62, v248
	v_readfirstlane_b32 s63, v249
	s_add_u32 s88, s88, s99
	s_addc_u32 s89, s89, 0
	s_add_u32 s62, s62, s99
	s_addc_u32 s63, s63, 0
	s_load_dwordx2 s[54:55], s[88:89], 0x0
	s_load_dwordx2 s[58:59], s[88:89], 0x8
	s_load_dwordx4 s[76:79], s[62:63], 0x0
.Lmy_gpre_skip:
	v_cndmask_b32_e64 v8, v1, v2, s[2:3]
	v_add_u32_e32 v2, -1, v1
	v_cmp_lt_i32_e64 s[4:5], s30, v2
	v_add_u32_e32 v0, s29, v0
	v_mov_b64_e32 v[16:17], s[24:25]
	v_cndmask_b32_e64 v12, v1, v2, s[4:5]
	v_mad_i64_i32 v[52:53], s[0:1], v0, s33, v[16:17]
	v_add_u32_e32 v0, s29, v8
	v_mad_i64_i32 v[56:57], s[0:1], v0, s33, v[16:17]
	v_add_u32_e32 v0, s29, v12
	v_add_u32_e32 v135, s29, v1
	v_and_b32_e32 v137, 3, v132
	s_lshl_b32 s52, s34, 8
	v_mad_i64_i32 v[60:61], s[0:1], v0, s33, v[16:17]
	v_mad_i64_i32 v[64:65], s[0:1], v135, s33, v[16:17]
	s_waitcnt lgkmcnt(0)
	v_lshl_add_u64 v[4:5], v[52:53], 0, s[52:53]
	v_lshlrev_b32_e32 v2, 6, v137
	v_lshl_add_u64 v[8:9], v[56:57], 0, s[52:53]
	v_lshl_add_u64 v[12:13], v[60:61], 0, s[52:53]
	v_lshl_add_u64 v[16:17], v[64:65], 0, s[52:53]
	v_lshl_add_u64 v[154:155], v[4:5], 0, v[2:3]
	v_lshl_add_u64 v[156:157], v[8:9], 0, v[2:3]
	v_lshl_add_u64 v[158:159], v[12:13], 0, v[2:3]
	v_lshl_add_u64 v[160:161], v[16:17], 0, v[2:3]
	global_load_dwordx4 v[4:7], v[154:155], off offset:3632
	global_load_dwordx4 v[20:23], v[154:155], off offset:3616
	global_load_dwordx4 v[36:39], v[154:155], off offset:3600
	global_load_dwordx4 v[116:119], v[154:155], off offset:3584
	global_load_dwordx4 v[8:11], v[156:157], off offset:3632
	global_load_dwordx4 v[24:27], v[156:157], off offset:3616
	global_load_dwordx4 v[40:43], v[156:157], off offset:3600
	global_load_dwordx4 v[120:123], v[156:157], off offset:3584
	global_load_dwordx4 v[12:15], v[158:159], off offset:3632
	global_load_dwordx4 v[28:31], v[158:159], off offset:3616
	global_load_dwordx4 v[44:47], v[158:159], off offset:3600
	global_load_dwordx4 v[124:127], v[158:159], off offset:3584
	global_load_dwordx4 v[16:19], v[160:161], off offset:3632
	global_load_dwordx4 v[32:35], v[160:161], off offset:3616
	global_load_dwordx4 v[48:51], v[160:161], off offset:3600
	global_load_dwordx4 v[128:131], v[160:161], off offset:3584
	s_add_i32 s0, s19, 0x20840
	v_mov_b32_e32 v0, s0
	s_add_i32 s0, s19, 0x20848
	ds_read2_b32 v[54:55], v0 offset1:1
	v_mov_b32_e32 v0, s0
	ds_read2_b32 v[58:59], v0 offset1:1
	s_add_i32 s36, s19, 0x19c00
	s_lshl_b32 s40, s34, 7
	s_lshl_b32 s39, s34, 1
	v_and_b32_e32 v133, 63, v132
	s_waitcnt lgkmcnt(1)
	v_readfirstlane_b32 s45, v54
	v_readfirstlane_b32 s43, v55
	s_waitcnt lgkmcnt(0)
	v_readfirstlane_b32 s42, v58
	s_cmp_gt_i32 s37, 1
	v_readfirstlane_b32 s44, v59
	s_cbranch_scc1 .LBB0_838
	s_add_i32 s1, s19, 0x20850
	v_lshl_or_b32 v54, v133, 1, s29
	v_mov_b32_e32 v0, s1
	v_ashrrev_i32_e32 v55, 31, v54
	ds_read2_b32 v[58:59], v0 offset1:1
	s_add_i32 s0, s37, s39
	v_lshlrev_b64 v[54:55], 6, v[54:55]
	v_lshl_add_u64 v[54:55], s[20:21], 0, v[54:55]
	s_ashr_i32 s1, s0, 31
	v_lshl_add_u64 v[54:55], s[0:1], 2, v[54:55]
	s_add_i32 s0, s0, s14
	s_mov_b64 s[6:7], 0x500010
	s_ashr_i32 s1, s0, 31
	v_lshl_add_u64 v[62:63], v[54:55], 0, s[6:7]
	s_waitcnt lgkmcnt(0)
	v_readfirstlane_b32 s46, v58
	s_lshl_b64 s[6:7], s[0:1], 2
	v_readfirstlane_b32 s47, v59
	s_add_u32 s0, s46, s6
	s_addc_u32 s1, s47, s7
	global_load_dword v0, v3, s[0:1]
	s_mov_b32 s0, 0x500000
	v_add_co_u32_e64 v54, s[0:1], s0, v54
	v_lshlrev_b32_e32 v90, 2, v133
	s_nop 0
	v_addc_co_u32_e64 v55, s[0:1], 0, v55, s[0:1]
	global_load_dword v58, v[54:55], off offset:16
	global_load_dword v59, v[62:63], off offset:64
	s_add_i32 s0, s19, 0x20858
	v_mov_b32_e32 v54, s0
	ds_read2_b32 v[54:55], v54 offset1:1
	s_waitcnt lgkmcnt(0)
	v_readfirstlane_b32 s0, v54
	v_readfirstlane_b32 s1, v55
	s_add_u32 s0, s0, s6
	s_addc_u32 s1, s1, s7
	v_add_u32_e32 v54, 0xfc, v90
	v_and_b32_e32 v91, 0xfc, v54
	v_cmp_gt_u32_e64 s[6:7], 2, v133
	global_load_dword v66, v3, s[0:1]
	s_waitcnt vmcnt(2)
	v_add_f32_e32 v54, v0, v58
	v_mul_f32_e64 v55, |v54|, s81
	s_waitcnt vmcnt(1)
	v_add_f32_e32 v0, v0, v59
	v_exp_f32_e32 v92, v55
	v_mul_f32_e64 v58, |v0|, s81
	v_exp_f32_e32 v93, v58
	v_max_f32_e32 v55, 0, v0
	v_add_f32_e32 v0, 1.0, v92
	v_frexp_mant_f32_e32 v69, v0
	v_cvt_f64_f32_e32 v[58:59], v0
	v_add_f32_e32 v67, 1.0, v93
	v_frexp_exp_i32_f64_e32 v58, v[58:59]
	v_cmp_gt_f32_e64 s[0:1], s87, v69
	v_add_f32_e32 v68, -1.0, v0
	v_frexp_mant_f32_e32 v71, v67
	v_cvt_f64_f32_e32 v[62:63], v67
	v_subbrev_co_u32_e64 v58, s[0:1], 0, v58, s[0:1]
	v_add_f32_e32 v70, -1.0, v67
	v_sub_f32_e32 v72, v68, v0
	v_frexp_exp_i32_f64_e32 v62, v[62:63]
	v_cmp_gt_f32_e64 s[0:1], s87, v71
	v_sub_f32_e32 v68, v92, v68
	v_sub_f32_e32 v59, v70, v67
	s_waitcnt vmcnt(0)
; #define LAS __attribute__((address_space(3)))
; DI float log_sigmoid_f(float x) { return fminf(x, 0.f) - log1pf(__expf(-fabsf(x))); }
; DI float softplus_f(float x) { return fmaxf(x, 0.f) + log1pf(__expf(-fabsf(x))); }
; DI void ssd_vectors(Frame& F, int l, int t0, int g, LAS float* DT, LAS float* AC, LAS float* RED) {
;     (void)RED;
;     if (F.wave < 2) {
;         const int r2 = F.wave, head = 2 * g + r2, s0 = 2 * F.lane; const float* gp = (const float*)(F.ws + WS_GATES) + (size_t)(t0 + s0) * 16 + 4 + head;
;         const float db = inp(F, I_DTB)[l * 4 + head], na = -__expf(inp(F, I_ALOG)[l * 4 + head]);
;         const float d0 = softplus_f(gp[0] + db), d1 = softplus_f(gp[16] + db); float a0 = na * d0, a1 = na * d1;
;         wscan2<false>(a0, a1, F.lane);
	v_mul_f32_e32 v63, 0x3fb8aa3b, v66
	v_add_f32_e32 v66, 1.0, v72
	v_subbrev_co_u32_e64 v62, s[0:1], 0, v62, s[0:1]
	v_sub_f32_e32 v70, v93, v70
	v_add_f32_e32 v59, 1.0, v59
	v_exp_f32_e32 v94, v63
	v_add_f32_e32 v63, v68, v66
	v_sub_u32_e32 v66, 0, v58
	v_sub_u32_e32 v69, 0, v62
	v_add_f32_e32 v68, v70, v59
	v_cvt_f32_i32_e32 v59, v62
	v_ldexp_f32 v62, v0, v66
	v_ldexp_f32 v66, v63, v66
	v_ldexp_f32 v63, v67, v69
	v_ldexp_f32 v67, v68, v69
	v_pk_add_f32 v[68:69], v[62:63], 1.0 op_sel_hi:[1,0]
	v_pk_add_f32 v[70:71], v[62:63], -1.0 op_sel_hi:[1,0]
	v_pk_add_f32 v[72:73], v[68:69], -1.0 op_sel_hi:[1,0]
	v_pk_add_f32 v[74:75], v[70:71], 1.0 op_sel_hi:[1,0]
	v_pk_add_f32 v[72:73], v[62:63], v[72:73] neg_lo:[0,1] neg_hi:[0,1]
	v_pk_add_f32 v[62:63], v[62:63], v[74:75] neg_lo:[0,1] neg_hi:[0,1]
	v_pk_add_f32 v[72:73], v[66:67], v[72:73]
	v_pk_add_f32 v[62:63], v[66:67], v[62:63]
	v_pk_add_f32 v[66:67], v[68:69], v[72:73]
	v_pk_add_f32 v[76:77], v[70:71], v[62:63]
	v_rcp_f32_e32 v78, v66
	v_rcp_f32_e32 v79, v67
	v_pk_add_f32 v[70:71], v[76:77], v[70:71] neg_lo:[0,1] neg_hi:[0,1]
	v_pk_add_f32 v[68:69], v[66:67], v[68:69] neg_lo:[0,1] neg_hi:[0,1]
	v_pk_add_f32 v[62:63], v[62:63], v[70:71] neg_lo:[0,1] neg_hi:[0,1]
	v_pk_mul_f32 v[70:71], v[76:77], v[78:79]
	v_pk_add_f32 v[68:69], v[72:73], v[68:69] neg_lo:[0,1] neg_hi:[0,1]
	v_pk_mul_f32 v[72:73], v[66:67], v[70:71]
	v_cvt_f32_i32_e32 v58, v58
	v_pk_fma_f32 v[80:81], v[70:71], v[66:67], v[72:73] neg_lo:[0,0,1] neg_hi:[0,0,1]
	s_mov_b32 s0, 0x3e9b6dac
	v_pk_fma_f32 v[80:81], v[70:71], v[68:69], v[80:81]
	v_pk_mul_f32 v[74:75], v[58:59], s[80:81] op_sel_hi:[1,0]
	v_pk_add_f32 v[82:83], v[72:73], v[80:81]
	v_max_f32_e32 v54, 0, v54
	v_pk_add_f32 v[84:85], v[76:77], v[82:83] neg_lo:[0,1] neg_hi:[0,1]
	v_pk_add_f32 v[72:73], v[82:83], v[72:73] neg_lo:[0,1] neg_hi:[0,1]
	v_pk_add_f32 v[76:77], v[76:77], v[84:85] neg_lo:[0,1] neg_hi:[0,1]
	v_pk_add_f32 v[72:73], v[72:73], v[80:81] neg_lo:[0,1] neg_hi:[0,1]
	v_pk_add_f32 v[76:77], v[76:77], v[82:83] neg_lo:[0,1] neg_hi:[0,1]
	s_nop 0
	v_pk_add_f32 v[62:63], v[62:63], v[76:77]
	s_nop 0
	v_pk_add_f32 v[62:63], v[72:73], v[62:63]
	s_nop 0
	v_pk_add_f32 v[72:73], v[84:85], v[62:63]
	s_nop 0
	v_pk_mul_f32 v[76:77], v[78:79], v[72:73]
	v_pk_add_f32 v[80:81], v[84:85], v[72:73] neg_lo:[0,1] neg_hi:[0,1]
	v_pk_mul_f32 v[82:83], v[66:67], v[76:77]
	v_pk_add_f32 v[62:63], v[62:63], v[80:81]
	v_pk_add_f32 v[80:81], v[70:71], v[76:77]
	v_pk_fma_f32 v[66:67], v[76:77], v[66:67], v[82:83] neg_lo:[0,0,1] neg_hi:[0,0,1]
	v_pk_add_f32 v[70:71], v[80:81], v[70:71] neg_lo:[0,1] neg_hi:[0,1]
	v_pk_fma_f32 v[66:67], v[76:77], v[68:69], v[66:67]
	v_pk_add_f32 v[68:69], v[76:77], v[70:71] neg_lo:[0,1] neg_hi:[0,1]
	v_pk_add_f32 v[70:71], v[82:83], v[66:67]
	s_nop 0
	v_pk_add_f32 v[76:77], v[70:71], v[82:83] neg_lo:[0,1] neg_hi:[0,1]
	v_pk_add_f32 v[82:83], v[72:73], v[70:71] neg_lo:[0,1] neg_hi:[0,1]
	v_pk_add_f32 v[66:67], v[76:77], v[66:67] neg_lo:[0,1] neg_hi:[0,1]
	v_pk_add_f32 v[72:73], v[72:73], v[82:83] neg_lo:[0,1] neg_hi:[0,1]
	v_pk_fma_f32 v[76:77], v[58:59], s[80:81], v[74:75] op_sel_hi:[1,0,1] neg_lo:[0,0,1] neg_hi:[0,0,1]
	v_pk_add_f32 v[70:71], v[72:73], v[70:71] neg_lo:[0,1] neg_hi:[0,1]
	s_nop 0
	v_pk_add_f32 v[62:63], v[62:63], v[70:71]
	s_nop 0
	v_pk_add_f32 v[62:63], v[66:67], v[62:63]
	s_nop 0
	v_pk_add_f32 v[62:63], v[82:83], v[62:63]
	v_mov_b32_e32 v83, v75
	v_pk_mul_f32 v[62:63], v[78:79], v[62:63]
	s_nop 0
	v_pk_add_f32 v[62:63], v[68:69], v[62:63]
	s_nop 0
	v_pk_add_f32 v[66:67], v[80:81], v[62:63]
	s_nop 0
	v_pk_add_f32 v[68:69], v[66:67], v[80:81] neg_lo:[0,1] neg_hi:[0,1]
	v_pk_mul_f32 v[72:73], v[66:67], v[66:67]
	v_pk_add_f32 v[62:63], v[62:63], v[68:69] neg_lo:[0,1] neg_hi:[0,1]
	v_pk_fma_f32 v[68:69], v[72:73], s[0:1], v[216:217] op_sel_hi:[1,0,0]
	s_mov_b32 s0, 0x3f2aaada
	v_ldexp_f32 v70, v66, 1
	v_ldexp_f32 v71, v67, 1
	v_pk_mul_f32 v[66:67], v[66:67], v[72:73]
	v_pk_fma_f32 v[68:69], v[72:73], v[68:69], s[0:1] op_sel_hi:[1,1,0]
	s_mov_b32 s0, 0xb102e308
	v_pk_mul_f32 v[66:67], v[66:67], v[68:69]
	v_ldexp_f32 v73, v63, 1
	v_pk_add_f32 v[68:69], v[70:71], v[66:67]
	v_pk_fma_f32 v[58:59], v[58:59], s[0:1], v[76:77] op_sel_hi:[1,0,1]
	v_pk_add_f32 v[70:71], v[68:69], v[70:71] neg_lo:[0,1] neg_hi:[0,1]
	v_ldexp_f32 v62, v62, 1
	v_pk_add_f32 v[66:67], v[66:67], v[70:71] neg_lo:[0,1] neg_hi:[0,1]
	v_mov_b32_e32 v70, v74
	v_mov_b32_e32 v71, v67
	v_mov_b32_e32 v72, v58
	v_mov_b32_e32 v63, v73
	v_pk_add_f32 v[70:71], v[70:71], v[72:73]
	v_pk_add_f32 v[72:73], v[62:63], v[66:67]
	v_mov_b32_e32 v67, v69
	v_mov_b32_e32 v63, v73
; DI float softplus_f(float x) { return fmaxf(x, 0.f) + log1pf(__expf(-fabsf(x))); }
; DI float shup(float v, int o, int lane) { return __int_as_float(__builtin_amdgcn_ds_bpermute(((lane - o) & 63) << 2, __float_as_int(v))); }
; template <bool IS_MAX> DI void wscan2(float& x0, float& x1, int lane) {
;     x1 = IS_MAX ? fmaxf(x0, x1) : x0 + x1;
;     float s = x1;
; #pragma unroll
;     for (int o = 1; o < 64; o <<= 1) { const float y = shup(s, o, lane); if (lane >= o) s = IS_MAX ? fmaxf(s, y) : s + y; }
;     const float ex = shup(s, 1, lane);
;     if (lane > 0) { x0 = IS_MAX ? fmaxf(x0, ex) : x0 + ex; x1 = IS_MAX ? fmaxf(x1, ex) : x1 + ex; }
; }
; DI void ssd_vectors(Frame& F, int l, int t0, int g, LAS float* DT, LAS float* AC, LAS float* RED) {
;     ...
;         const float db = inp(F, I_DTB)[l * 4 + head], na = -__expf(inp(F, I_ALOG)[l * 4 + head]);
;         const float d0 = softplus_f(gp[0] + db), d1 = softplus_f(gp[16] + db); float a0 = na * d0, a1 = na * d1;
;         wscan2<false>(a0, a1, F.lane);
;         DT[r2 * 128 + s0] = d0; DT[r2 * 128 + s0 + 1] = d1; AC[r2 * 128 + s0] = a0; AC[r2 * 128 + s0 + 1] = a1; }
;     __syncthreads();
	v_pk_add_f32 v[76:77], v[74:75], v[58:59]
	v_pk_add_f32 v[62:63], v[62:63], v[66:67]
	v_pk_add_f32 v[66:67], v[68:69], v[72:73]
	v_mov_b32_e32 v86, v68
	v_pk_add_f32 v[78:79], v[76:77], v[66:67]
	v_mov_b32_e32 v84, v66
	v_mov_b32_e32 v85, v79
	v_mov_b32_e32 v87, v77
	v_pk_add_f32 v[84:85], v[84:85], v[86:87] neg_lo:[0,1] neg_hi:[0,1]
	v_mov_b32_e32 v80, v78
	v_mov_b32_e32 v81, v77
	v_mov_b32_e32 v82, v76
	v_mov_b32_e32 v86, v76
	v_mov_b32_e32 v87, v79
	v_mov_b32_e32 v75, v85
	v_pk_add_f32 v[80:81], v[80:81], v[82:83] neg_lo:[0,1] neg_hi:[0,1]
	v_mov_b32_e32 v82, v66
	v_mov_b32_e32 v83, v59
	v_pk_add_f32 v[74:75], v[86:87], v[74:75] neg_lo:[0,1] neg_hi:[0,1]
	v_pk_add_f32 v[82:83], v[82:83], v[80:81] neg_lo:[0,1] neg_hi:[0,1]
	v_mov_b32_e32 v86, v74
	v_mov_b32_e32 v87, v81
	v_mov_b32_e32 v88, v78
	v_mov_b32_e32 v89, v67
	v_mov_b32_e32 v81, v69
	v_pk_add_f32 v[86:87], v[58:59], v[86:87] neg_lo:[0,1] neg_hi:[0,1]
	v_pk_add_f32 v[80:81], v[88:89], v[80:81] neg_lo:[0,1] neg_hi:[0,1]
	v_mov_b32_e32 v59, v77
	v_pk_add_f32 v[66:67], v[66:67], v[68:69] neg_lo:[0,1] neg_hi:[0,1]
	v_pk_add_f32 v[68:69], v[70:71], v[80:81] neg_lo:[0,1] neg_hi:[0,1]
	v_pk_add_f32 v[58:59], v[58:59], v[74:75] neg_lo:[0,1] neg_hi:[0,1]
	v_pk_add_f32 v[62:63], v[62:63], v[84:85] neg_lo:[0,1] neg_hi:[0,1]
	v_pk_add_f32 v[66:67], v[72:73], v[66:67] neg_lo:[0,1] neg_hi:[0,1]
	v_pk_add_f32 v[70:71], v[62:63], v[58:59]
	v_mov_b32_e32 v59, v83
	v_mov_b32_e32 v63, v69
	v_pk_add_f32 v[72:73], v[82:83], v[68:69]
	v_pk_add_f32 v[62:63], v[58:59], v[62:63]
	v_mov_b32_e32 v68, v70
	v_pk_add_f32 v[62:63], v[62:63], v[86:87] neg_lo:[0,1] neg_hi:[0,1]
	v_mov_b32_e32 v69, v73
	v_pk_add_f32 v[68:69], v[68:69], v[62:63] neg_lo:[0,1] neg_hi:[0,1]
	v_pk_add_f32 v[62:63], v[66:67], v[62:63] neg_lo:[0,1] neg_hi:[0,1]
	v_pk_add_f32 v[58:59], v[58:59], v[68:69] neg_lo:[0,1] neg_hi:[0,1]
	v_cmp_neq_f32_e64 s[0:1], s82, v92
	v_pk_add_f32 v[58:59], v[62:63], v[58:59]
	v_pk_add_f32 v[62:63], v[72:73], v[70:71]
	s_nop 0
	v_pk_add_f32 v[66:67], v[78:79], v[62:63]
	s_nop 0
	v_pk_add_f32 v[68:69], v[66:67], v[78:79] neg_lo:[0,1] neg_hi:[0,1]
	s_nop 0
	v_pk_add_f32 v[62:63], v[62:63], v[68:69] neg_lo:[0,1] neg_hi:[0,1]
	s_nop 0
	v_pk_add_f32 v[58:59], v[58:59], v[62:63]
	v_add_u32_e32 v62, 0xf8, v90
	v_pk_add_f32 v[58:59], v[66:67], v[58:59]
	v_and_b32_e32 v62, 0xfc, v62
	v_cndmask_b32_e64 v0, v230, v58, s[0:1]
	v_cmp_neq_f32_e64 s[0:1], s82, v93
	v_add_u32_e32 v63, 0xf0, v90
	v_and_b32_e32 v63, 0xfc, v63
	v_cndmask_b32_e64 v58, v230, v59, s[0:1]
	v_cmp_ngt_f32_e64 s[0:1], -1.0, v93
	s_nop 1
	v_cndmask_b32_e64 v58, v231, v58, s[0:1]
	v_cmp_ngt_f32_e64 s[0:1], -1.0, v92
	s_nop 1
	v_cndmask_b32_e64 v0, v231, v0, s[0:1]
	v_cmp_neq_f32_e64 s[0:1], -1.0, v92
	s_nop 1
	v_cndmask_b32_e64 v0, v232, v0, s[0:1]
	v_cmp_neq_f32_e64 s[0:1], -1.0, v93
	s_nop 1
	v_cndmask_b32_e64 v58, v232, v58, s[0:1]
	v_cmp_lt_f32_e64 s[0:1], |v93|, s86
	s_nop 1
	v_cndmask_b32_e64 v59, v58, v93, s[0:1]
	v_cmp_lt_f32_e64 s[0:1], |v92|, s86
	s_nop 1
	v_cndmask_b32_e64 v58, v0, v92, s[0:1]
	v_pk_add_f32 v[54:55], v[54:55], v[58:59]
	v_cmp_eq_u32_e64 s[0:1], 0, v133
	v_mul_f32_e64 v0, v54, -v94
	v_fma_f32 v58, -v94, v55, v0
	ds_bpermute_b32 v59, v91, v58
	s_waitcnt lgkmcnt(0)
	v_add_f32_e32 v59, v58, v59
	v_cndmask_b32_e64 v59, v59, v58, s[0:1]
	ds_bpermute_b32 v62, v62, v59
	s_waitcnt lgkmcnt(0)
	v_add_f32_e32 v62, v59, v62
	v_cndmask_b32_e64 v59, v62, v59, s[6:7]
	ds_bpermute_b32 v62, v63, v59
	v_add_u32_e32 v63, 0xe0, v90
	v_cmp_gt_u32_e64 s[6:7], 4, v133
	v_and_b32_e32 v63, 0xfc, v63
	s_waitcnt lgkmcnt(0)
	v_add_f32_e32 v62, v59, v62
	v_cndmask_b32_e64 v59, v62, v59, s[6:7]
	ds_bpermute_b32 v62, v63, v59
	v_add_u32_e32 v63, 0xc0, v90
	v_cmp_gt_u32_e64 s[6:7], 8, v133
	v_and_b32_e32 v63, 0xfc, v63
	s_waitcnt lgkmcnt(0)
	v_add_f32_e32 v62, v59, v62
	v_cndmask_b32_e64 v59, v62, v59, s[6:7]
	ds_bpermute_b32 v62, v63, v59
	v_cmp_gt_u32_e64 s[6:7], 16, v133
	v_xor_b32_e32 v63, 0x80, v90
	s_waitcnt lgkmcnt(0)
	v_add_f32_e32 v62, v59, v62
	v_cndmask_b32_e64 v59, v62, v59, s[6:7]
	ds_bpermute_b32 v62, v63, v59
	v_cmp_gt_u32_e64 s[6:7], 32, v133
	s_waitcnt lgkmcnt(0)
	v_add_f32_e32 v62, v59, v62
	v_cndmask_b32_e64 v59, v62, v59, s[6:7]
	ds_bpermute_b32 v59, v91, v59
	v_lshlrev_b32_e32 v62, 3, v133
	v_lshl_or_b32 v62, s37, 9, v62
	v_add_u32_e32 v63, s41, v62
	ds_write2_b32 v63, v54, v55 offset1:1
	s_waitcnt lgkmcnt(1)
	v_fma_f32 v66, v54, -v94, v59
	v_add_f32_e32 v59, v58, v59
	v_cndmask_b32_e64 v0, v66, v0, s[0:1]
	v_cndmask_b32_e64 v58, v59, v58, s[0:1]
	v_add_u32_e32 v54, s36, v62
	ds_write2_b32 v54, v0, v58 offset1:1

; #define LAS __attribute__((address_space(3)))
; DI float log_sigmoid_f(float x) { return fminf(x, 0.f) - log1pf(__expf(-fabsf(x))); }
; DI void ml_vectors(Frame& F, int l, int t0, int h, LAS float* A, LAS float* IG, LAS float* RED) {
;     (void)RED;
;     if (F.wave == 0) {
;         const int s0 = 2 * F.lane; const float* gp = (const float*)(F.ws + WS_GATES) + (size_t)(t0 + s0) * 16; const float fb = inp(F, I_FB)[l * 4 + h], ib = inp(F, I_IB)[l * 4 + h];
;         float a0 = log_sigmoid_f(gp[12 + h] + fb), a1 = log_sigmoid_f(gp[16 + 12 + h] + fb);
;         IG[s0] = gp[8 + h] + ib; IG[s0 + 1] = gp[16 + 8 + h] + ib;
.LBB0_845:
	v_and_b32_e32 v0, -2, v1
	s_ashr_i32 s17, s16, 31
	s_lshl_b64 s[2:3], s[16:17], 7
	v_ashrrev_i32_e32 v1, 31, v0
	v_lshl_add_u64 v[0:1], s[2:3], 0, v[0:1]
	v_mov_b64_e32 v[4:5], s[24:25]
	v_mad_u64_u32 v[4:5], s[0:1], v0, s33, v[4:5]
	v_lshlrev_b32_e32 v0, 4, v132
	v_mad_i32_i24 v5, v1, s33, v5
	v_and_b32_e32 v2, 0x70, v0
	v_lshl_add_u64 v[0:1], v[4:5], 0, v[2:3]
	v_add_co_u32_e32 v8, vcc, s64, v0
	s_movk_i32 s0, 0x3000
	s_nop 0
	v_addc_co_u32_e32 v9, vcc, 0, v1, vcc
	v_add_co_u32_e32 v4, vcc, s0, v0
	s_mov_b64 s[0:1], 0
	s_nop 0
	v_addc_co_u32_e32 v5, vcc, 0, v1, vcc
	v_add_co_u32_e32 v0, vcc, s6, v0
	s_mov_b32 s7, s53
	s_nop 0
	v_addc_co_u32_e32 v1, vcc, 0, v1, vcc
	global_load_dwordx4 v[20:23], v[8:9], off offset:1536
	global_load_dwordx4 v[24:27], v[8:9], off offset:1664
	global_load_dwordx4 v[28:31], v[4:5], off
	global_load_dwordx4 v[32:35], v[4:5], off offset:128
	s_nop 0
	global_load_dwordx4 v[4:7], v[8:9], off offset:1024
	global_load_dwordx4 v[12:15], v[8:9], off offset:1152
	s_nop 0
	global_load_dwordx4 v[8:11], v[0:1], off offset:3584
	global_load_dwordx4 v[16:19], v[0:1], off offset:3712
	s_add_u32 s4, s20, s0
	v_and_b32_e32 v1, 63, v132
	v_readfirstlane_b32 s6, v132
	s_addc_u32 s5, s21, s1
	s_add_i32 s17, s19, s7
	v_lshlrev_b32_e32 v41, 2, v1
	s_cmp_gt_u32 s6, 63
	v_cmp_eq_u32_e32 vcc, 0, v1
	v_xor_b32_e32 v40, 0x80, v41
	s_cbranch_scc1 .LBB0_847
	v_lshl_or_b32 v36, v1, 1, s29
	v_ashrrev_i32_e32 v37, 31, v36
	v_lshlrev_b64 v[36:37], 6, v[36:37]
	v_lshl_add_u64 v[36:37], s[4:5], 0, v[36:37]
	s_mov_b64 s[0:1], 0x500000
	v_lshl_add_u64 v[36:37], v[36:37], 0, s[0:1]
	s_add_i32 s0, s17, 0x20870
	v_mov_b32_e32 v0, s0
	ds_read2_b32 v[38:39], v0 offset1:1
	s_lshl_b64 s[0:1], s[14:15], 2
	s_waitcnt lgkmcnt(0)
	v_readfirstlane_b32 s7, v38
	v_readfirstlane_b32 s19, v39
	s_add_u32 s20, s7, s0
	s_addc_u32 s21, s19, s1
	s_add_i32 s7, s17, 0x20868
	v_mov_b32_e32 v0, s7
	ds_read2_b32 v[42:43], v0 offset1:1
	v_mov_b32_e32 v38, s76
	s_waitcnt lgkmcnt(0)
	v_readfirstlane_b32 s7, v42
	v_readfirstlane_b32 s19, v43
	s_add_u32 s0, s7, s0
	s_addc_u32 s1, s19, s1
	v_mov_b32_e32 v2, s54
	s_waitcnt vmcnt(8)
	v_mov_b32_e32 v0, v224
	v_mov_b32_e32 v153, v218
	v_mov_b32_e32 v152, v238
	v_mov_b32_e32 v151, v242
	s_nop 0
	v_add_f32_e32 v0, v38, v0
	v_min_f32_e32 v39, 0, v0
	v_mul_f32_e64 v0, |v0|, s81
	v_exp_f32_e32 v0, v0
	s_nop 0
	v_add_f32_e32 v44, 1.0, v0
	v_add_f32_e32 v42, -1.0, v44
	v_sub_f32_e32 v43, v42, v44
	v_add_f32_e32 v43, 1.0, v43
	v_sub_f32_e32 v42, v0, v42
	v_add_f32_e32 v45, v42, v43
	v_frexp_mant_f32_e32 v42, v44
	v_cmp_gt_f32_e64 s[0:1], s87, v42
	v_cvt_f64_f32_e32 v[42:43], v44
	v_frexp_exp_i32_f64_e32 v42, v[42:43]
	v_subbrev_co_u32_e64 v42, s[0:1], 0, v42, s[0:1]
	v_sub_u32_e32 v43, 0, v42
	v_ldexp_f32 v44, v44, v43
	v_ldexp_f32 v43, v45, v43
	v_add_f32_e32 v45, -1.0, v44
	v_add_f32_e32 v46, 1.0, v45
	v_sub_f32_e32 v46, v44, v46
	v_add_f32_e32 v46, v43, v46
	v_add_f32_e32 v47, v45, v46
	v_sub_f32_e32 v45, v47, v45
	v_sub_f32_e32 v45, v46, v45
	v_add_f32_e32 v46, 1.0, v44
	v_add_f32_e32 v48, -1.0, v46
	v_sub_f32_e32 v44, v44, v48
	v_add_f32_e32 v43, v43, v44
	v_add_f32_e32 v44, v46, v43
	v_sub_f32_e32 v46, v44, v46
	v_sub_f32_e32 v43, v43, v46
	v_rcp_f32_e32 v46, v44
	v_cvt_f32_i32_e32 v42, v42
	v_cmp_neq_f32_e64 s[0:1], s82, v0
	v_mul_f32_e32 v48, v47, v46
	v_mul_f32_e32 v49, v44, v48
	v_fma_f32 v50, v48, v44, -v49
	v_fmac_f32_e32 v50, v48, v43
	v_add_f32_e32 v51, v49, v50
	v_sub_f32_e32 v52, v47, v51
	v_sub_f32_e32 v47, v47, v52
	v_sub_f32_e32 v49, v51, v49
	v_sub_f32_e32 v47, v47, v51
	v_add_f32_e32 v45, v45, v47
	v_sub_f32_e32 v47, v49, v50
	v_add_f32_e32 v45, v47, v45
	v_add_f32_e32 v47, v52, v45
	v_mul_f32_e32 v49, v46, v47
	v_mul_f32_e32 v50, v44, v49
	v_fma_f32 v44, v49, v44, -v50
	v_fmac_f32_e32 v44, v49, v43
	v_sub_f32_e32 v43, v52, v47
	v_add_f32_e32 v43, v45, v43
	v_add_f32_e32 v45, v50, v44
	v_sub_f32_e32 v51, v47, v45
	v_sub_f32_e32 v47, v47, v51
	v_sub_f32_e32 v50, v45, v50
	v_sub_f32_e32 v45, v47, v45
	v_add_f32_e32 v43, v43, v45
	v_sub_f32_e32 v44, v50, v44
	v_add_f32_e32 v43, v44, v43
	v_add_f32_e32 v44, v48, v49
	v_add_f32_e32 v43, v51, v43
	v_sub_f32_e32 v45, v44, v48
	v_mul_f32_e32 v43, v46, v43
	v_sub_f32_e32 v45, v49, v45
	v_add_f32_e32 v43, v45, v43
	v_mul_f32_e32 v48, 0x3f317218, v42
	v_add_f32_e32 v45, v44, v43
	v_fma_f32 v49, v42, s80, -v48
	v_mul_f32_e32 v46, v45, v45
	v_fmac_f32_e32 v49, 0xb102e308, v42
	v_sub_f32_e32 v42, v45, v44
	v_fmamk_f32 v47, v46, 0x3e9b6dac, v216
	v_sub_f32_e32 v42, v43, v42
	v_add_f32_e32 v43, v48, v49
	v_fmaak_f32 v47, v46, v47, 0x3f2aaada
	v_sub_f32_e32 v44, v43, v48
	v_ldexp_f32 v48, v45, 1
	v_mul_f32_e32 v45, v45, v46
	v_mul_f32_e32 v45, v45, v47
	v_add_f32_e32 v46, v48, v45
	v_sub_f32_e32 v47, v46, v48
	v_ldexp_f32 v42, v42, 1
	v_sub_f32_e32 v45, v45, v47
	v_add_f32_e32 v42, v42, v45
	v_add_f32_e32 v45, v46, v42
	v_sub_f32_e32 v46, v45, v46
	v_sub_f32_e32 v42, v42, v46
	v_add_f32_e32 v46, v43, v45
	v_sub_f32_e32 v47, v46, v43
	v_sub_f32_e32 v48, v46, v47
	v_sub_f32_e32 v44, v49, v44
	v_sub_f32_e32 v43, v43, v48
	v_sub_f32_e32 v45, v45, v47
	v_add_f32_e32 v43, v45, v43
	v_add_f32_e32 v45, v44, v42
	v_sub_f32_e32 v47, v45, v44
	v_sub_f32_e32 v48, v45, v47
	v_sub_f32_e32 v44, v44, v48
	v_sub_f32_e32 v42, v42, v47
	v_add_f32_e32 v43, v45, v43
	v_add_f32_e32 v42, v42, v44
	v_add_f32_e32 v44, v46, v43
	v_sub_f32_e32 v45, v44, v46
	v_sub_f32_e32 v43, v43, v45
	v_add_f32_e32 v42, v42, v43
	v_add_f32_e32 v42, v44, v42
	v_cndmask_b32_e64 v42, v230, v42, s[0:1]
; #define LAS __attribute__((address_space(3)))
; DI float log_sigmoid_f(float x) { return fminf(x, 0.f) - log1pf(__expf(-fabsf(x))); }
; DI float shup(float v, int o, int lane) { return __int_as_float(__builtin_amdgcn_ds_bpermute(((lane - o) & 63) << 2, __float_as_int(v))); }
; template <bool IS_MAX> DI void wscan2(float& x0, float& x1, int lane) {
;     x1 = IS_MAX ? fmaxf(x0, x1) : x0 + x1;
;     float s = x1;
; #pragma unroll
;     for (int o = 1; o < 64; o <<= 1) { const float y = shup(s, o, lane); if (lane >= o) s = IS_MAX ? fmaxf(s, y) : s + y; }
;     const float ex = shup(s, 1, lane);
;     if (lane > 0) { x0 = IS_MAX ? fmaxf(x0, ex) : x0 + ex; x1 = IS_MAX ? fmaxf(x1, ex) : x1 + ex; }
; }
; DI void ml_vectors(Frame& F, int l, int t0, int h, LAS float* A, LAS float* IG, LAS float* RED) {
;     (void)RED;
;     if (F.wave == 0) {
;         const int s0 = 2 * F.lane; const float* gp = (const float*)(F.ws + WS_GATES) + (size_t)(t0 + s0) * 16; const float fb = inp(F, I_FB)[l * 4 + h], ib = inp(F, I_IB)[l * 4 + h];
;         float a0 = log_sigmoid_f(gp[12 + h] + fb), a1 = log_sigmoid_f(gp[16 + 12 + h] + fb);
;         IG[s0] = gp[8 + h] + ib; IG[s0 + 1] = gp[16 + 8 + h] + ib;
;         wscan2<false>(a0, a1, F.lane);
;         A[s0] = a0; A[s0 + 1] = a1; }
;     __syncthreads();
; }
	v_cmp_ngt_f32_e64 s[0:1], -1.0, v0
	s_nop 1
	v_cndmask_b32_e64 v42, v231, v42, s[0:1]
	v_cmp_neq_f32_e64 s[0:1], -1.0, v0
	s_nop 1
	v_cndmask_b32_e64 v42, v232, v42, s[0:1]
	v_cmp_lt_f32_e64 s[0:1], |v0|, s86
	s_nop 1
	v_cndmask_b32_e64 v0, v42, v0, s[0:1]
	v_sub_f32_e32 v42, v39, v0
	v_add_f32_e32 v0, v38, v151
	v_min_f32_e32 v43, 0, v0
	v_mul_f32_e64 v0, |v0|, s81
	v_exp_f32_e32 v0, v0
	s_nop 0
	v_add_f32_e32 v44, 1.0, v0
	v_add_f32_e32 v38, -1.0, v44
	v_sub_f32_e32 v39, v38, v44
	v_add_f32_e32 v39, 1.0, v39
	v_sub_f32_e32 v38, v0, v38
	v_add_f32_e32 v45, v38, v39
	v_frexp_mant_f32_e32 v38, v44
	v_cmp_gt_f32_e64 s[0:1], s87, v38
	v_cvt_f64_f32_e32 v[38:39], v44
	v_frexp_exp_i32_f64_e32 v38, v[38:39]
	v_subbrev_co_u32_e64 v38, s[0:1], 0, v38, s[0:1]
	v_sub_u32_e32 v39, 0, v38
	v_ldexp_f32 v44, v44, v39
	v_ldexp_f32 v39, v45, v39
	v_add_f32_e32 v45, -1.0, v44
	v_add_f32_e32 v46, 1.0, v45
	v_sub_f32_e32 v46, v44, v46
	v_add_f32_e32 v46, v39, v46
	v_add_f32_e32 v47, v45, v46
	v_sub_f32_e32 v45, v47, v45
	v_sub_f32_e32 v45, v46, v45
	v_add_f32_e32 v46, 1.0, v44
	v_add_f32_e32 v48, -1.0, v46
	v_sub_f32_e32 v44, v44, v48
	v_add_f32_e32 v39, v39, v44
	v_add_f32_e32 v44, v46, v39
	v_sub_f32_e32 v46, v44, v46
	v_sub_f32_e32 v39, v39, v46
	v_rcp_f32_e32 v46, v44
	v_cvt_f32_i32_e32 v38, v38
	v_cmp_neq_f32_e64 s[0:1], s82, v0
	v_mul_f32_e32 v48, v47, v46
	v_mul_f32_e32 v49, v44, v48
	v_fma_f32 v50, v48, v44, -v49
	v_fmac_f32_e32 v50, v48, v39
	v_add_f32_e32 v51, v49, v50
	v_sub_f32_e32 v52, v47, v51
	v_sub_f32_e32 v47, v47, v52
	v_sub_f32_e32 v49, v51, v49
	v_sub_f32_e32 v47, v47, v51
	v_add_f32_e32 v45, v45, v47
	v_sub_f32_e32 v47, v49, v50
	v_add_f32_e32 v45, v47, v45
	v_add_f32_e32 v47, v52, v45
	v_mul_f32_e32 v49, v46, v47
	v_mul_f32_e32 v50, v44, v49
	v_fma_f32 v44, v49, v44, -v50
	v_fmac_f32_e32 v44, v49, v39
	v_sub_f32_e32 v39, v52, v47
	v_add_f32_e32 v39, v45, v39
	v_add_f32_e32 v45, v50, v44
	v_sub_f32_e32 v51, v47, v45
	v_sub_f32_e32 v47, v47, v51
	v_sub_f32_e32 v50, v45, v50
	v_sub_f32_e32 v45, v47, v45
	v_add_f32_e32 v39, v39, v45
	v_sub_f32_e32 v44, v50, v44
	v_add_f32_e32 v39, v44, v39
	v_add_f32_e32 v44, v48, v49
	v_add_f32_e32 v39, v51, v39
	v_sub_f32_e32 v45, v44, v48
	v_mul_f32_e32 v39, v46, v39
	v_sub_f32_e32 v45, v49, v45
	v_add_f32_e32 v39, v45, v39
	v_mul_f32_e32 v48, 0x3f317218, v38
	v_add_f32_e32 v45, v44, v39
	v_fma_f32 v49, v38, s80, -v48
	v_mul_f32_e32 v46, v45, v45
	v_fmac_f32_e32 v49, 0xb102e308, v38
	v_sub_f32_e32 v38, v45, v44
	v_fmamk_f32 v47, v46, 0x3e9b6dac, v216
	v_sub_f32_e32 v38, v39, v38
	v_add_f32_e32 v39, v48, v49
	v_fmaak_f32 v47, v46, v47, 0x3f2aaada
	v_sub_f32_e32 v44, v39, v48
	v_ldexp_f32 v48, v45, 1
	v_mul_f32_e32 v45, v45, v46
	v_mul_f32_e32 v45, v45, v47
	v_add_f32_e32 v46, v48, v45
	v_sub_f32_e32 v47, v46, v48
	v_ldexp_f32 v38, v38, 1
	v_sub_f32_e32 v45, v45, v47
	v_add_f32_e32 v38, v38, v45
	v_add_f32_e32 v45, v46, v38
	v_sub_f32_e32 v46, v45, v46
	v_sub_f32_e32 v38, v38, v46
	v_add_f32_e32 v46, v39, v45
	v_sub_f32_e32 v47, v46, v39
	v_sub_f32_e32 v48, v46, v47
	v_sub_f32_e32 v44, v49, v44
	v_sub_f32_e32 v39, v39, v48
	v_sub_f32_e32 v45, v45, v47
	v_add_f32_e32 v39, v45, v39
	v_add_f32_e32 v45, v44, v38
	v_sub_f32_e32 v47, v45, v44
	v_sub_f32_e32 v48, v45, v47
	v_sub_f32_e32 v44, v44, v48
	v_sub_f32_e32 v38, v38, v47
	v_add_f32_e32 v39, v45, v39
	v_add_f32_e32 v38, v38, v44
	v_add_f32_e32 v44, v46, v39
	v_sub_f32_e32 v45, v44, v46
	v_sub_f32_e32 v39, v39, v45
	v_add_f32_e32 v38, v38, v39
	v_add_f32_e32 v38, v44, v38
	v_cndmask_b32_e64 v38, v230, v38, s[0:1]
	v_cmp_ngt_f32_e64 s[0:1], -1.0, v0
	v_mov_b32_e32 v39, v152
	s_nop 0
	v_cndmask_b32_e64 v38, v231, v38, s[0:1]
	v_cmp_neq_f32_e64 s[0:1], -1.0, v0
	s_nop 1
	v_cndmask_b32_e64 v38, v232, v38, s[0:1]
	v_cmp_lt_f32_e64 s[0:1], |v0|, s86
	s_nop 1
	v_cndmask_b32_e64 v0, v38, v0, s[0:1]
	v_mov_b32_e32 v38, v153
	v_sub_f32_e32 v44, v43, v0
	v_lshl_add_u32 v43, v1, 3, s17
	v_add_u32_e32 v45, 0x9b00, v43
	v_add_f32_e32 v0, v42, v44
	v_cmp_gt_u32_e64 s[0:1], 2, v1
	s_nop 0
	v_pk_add_f32 v[36:37], v[2:3], v[38:39] op_sel_hi:[0,1]
	v_add_u32_e32 v2, 0xfc, v41
	v_and_b32_e32 v2, 0xfc, v2
	ds_write2_b32 v45, v36, v37 offset1:1
	ds_bpermute_b32 v36, v2, v0
	v_add_u32_e32 v37, 0xf8, v41
	v_and_b32_e32 v37, 0xfc, v37
	s_waitcnt lgkmcnt(0)
	v_add_f32_e32 v36, v0, v36
	v_cndmask_b32_e32 v36, v36, v0, vcc
	ds_bpermute_b32 v37, v37, v36
	s_waitcnt lgkmcnt(0)
	v_add_f32_e32 v37, v36, v37
	v_cndmask_b32_e64 v36, v37, v36, s[0:1]
	v_add_u32_e32 v37, 0xf0, v41
	v_and_b32_e32 v37, 0xfc, v37
	ds_bpermute_b32 v37, v37, v36
	v_cmp_gt_u32_e64 s[0:1], 4, v1
	s_waitcnt lgkmcnt(0)
	v_add_f32_e32 v37, v36, v37
	v_cndmask_b32_e64 v36, v37, v36, s[0:1]
	v_add_u32_e32 v37, 0xe0, v41
	v_and_b32_e32 v37, 0xfc, v37
	ds_bpermute_b32 v37, v37, v36
	v_cmp_gt_u32_e64 s[0:1], 8, v1
	s_waitcnt lgkmcnt(0)
	v_add_f32_e32 v37, v36, v37
	v_cndmask_b32_e64 v36, v37, v36, s[0:1]
	v_add_u32_e32 v37, 0xc0, v41
	v_and_b32_e32 v37, 0xfc, v37
	ds_bpermute_b32 v37, v37, v36
	v_cmp_gt_u32_e64 s[0:1], 16, v1
	s_waitcnt lgkmcnt(0)
	v_add_f32_e32 v37, v36, v37
	v_cndmask_b32_e64 v36, v37, v36, s[0:1]
	ds_bpermute_b32 v37, v40, v36
	v_cmp_gt_u32_e64 s[0:1], 32, v1
	s_waitcnt lgkmcnt(0)
	v_add_f32_e32 v37, v36, v37
	v_cndmask_b32_e64 v36, v37, v36, s[0:1]
	ds_bpermute_b32 v2, v2, v36
	s_waitcnt lgkmcnt(0)
	v_add_f32_e32 v36, v42, v2
	v_add_f32_e32 v2, v0, v2
	v_cndmask_b32_e32 v36, v36, v42, vcc
	v_cndmask_b32_e32 v0, v2, v0, vcc
	v_add_u32_e32 v2, 0x9900, v43
	ds_write2_b32 v2, v36, v0 offset1:1

; #define LAS __attribute__((address_space(3)))
; DI float log_sigmoid_f(float x) { return fminf(x, 0.f) - log1pf(__expf(-fabsf(x))); }
; DI void refresh(Frame& F) { int t_ = F.tid; asm volatile("" : "+v"(t_)); F.tid = t_; F.lane = t_ & 63; F.wave = __builtin_amdgcn_readfirstlane(t_ >> 6); size_t z_ = 0; unsigned zl_ = 0; asm volatile("" : "+s"(z_), "+s"(zl_)); F.ws = F.ws + z_; F.lds = F.lds + zl_; }
; DI void ml_vectors(Frame& F, int l, int t0, int h, LAS float* A, LAS float* IG, LAS float* RED) {
;     (void)RED;
;     if (F.wave == 0) {
;         const int s0 = 2 * F.lane; const float* gp = (const float*)(F.ws + WS_GATES) + (size_t)(t0 + s0) * 16; const float fb = inp(F, I_FB)[l * 4 + h], ib = inp(F, I_IB)[l * 4 + h];
;         float a0 = log_sigmoid_f(gp[12 + h] + fb), a1 = log_sigmoid_f(gp[16 + 12 + h] + fb);
;         IG[s0] = gp[8 + h] + ib; IG[s0 + 1] = gp[16 + 8 + h] + ib;
;         wscan2<false>(a0, a1, F.lane);
;         A[s0] = a0; A[s0 + 1] = a1; }
;     __syncthreads();
; }
; DI void ml_local_unit(Frame& F, int l, int ch, int h, const MlLPre& P) {
;     refresh(F);
;     LAS bf16* VWT = (LAS bf16*)F.lds;
;     LAS bf16* KT = VWT + 80 * LP;
;     LAS float* A = (LAS float*)(F.lds + (80 + 64) * LP * 2); LAS float* IG = A + 128; LAS float* WG = IG + 128; LAS float* RED = WG + 128;
;     const int t0 = ch * CHUNK; const bf16* proj = (const bf16*)(F.ws + WS_PROJ);
;     const int s2 = (F.tid >> 3) * 2, c0 = (F.tid & 7) * 8; (void)proj;
;     const v4u rv0 = P.v0, rv1 = P.v1, rk0 = P.k0, rk1 = P.k1;
;     ml_vectors(F, l, t0, h, A, IG, RED);
.LBB0_867:
	s_or_b64 exec, exec, s[0:1]
	v_ashrrev_i32_e32 v39, 31, v38
	v_lshl_add_u64 v[0:1], s[2:3], 0, v[38:39]
	v_mov_b64_e32 v[4:5], s[4:5]
	v_mad_u64_u32 v[4:5], s[0:1], v0, s33, v[4:5]
	v_mad_i32_i24 v5, v1, s33, v5
	v_lshlrev_b32_e32 v2, 1, v40
	v_lshl_add_u64 v[0:1], v[4:5], 0, v[2:3]
	s_mov_b32 s0, 0xb101000
	v_add_co_u32_e32 v4, vcc, s0, v0
	s_mov_b32 s0, 0xb103000
	s_nop 0
	v_addc_co_u32_e32 v5, vcc, 0, v1, vcc
	v_add_co_u32_e32 v8, vcc, s0, v0
	s_mov_b32 s0, 0xb102000
	s_nop 0
	v_addc_co_u32_e32 v9, vcc, 0, v1, vcc
	v_add_co_u32_e32 v0, vcc, s0, v0
	s_barrier
	global_load_dwordx4 v[20:23], v[4:5], off offset:1792
	s_nop 0
	global_load_dwordx4 v[4:7], v[4:5], off offset:1280
	v_addc_co_u32_e32 v1, vcc, 0, v1, vcc
	global_load_dwordx4 v[28:31], v[8:9], off offset:256
	s_nop 0
	global_load_dwordx4 v[8:11], v[0:1], off offset:3840
	s_mov_b64 s[0:1], 0
	s_mov_b32 s7, s53
	s_add_u32 s4, s4, s0
	v_and_b32_e32 v1, 63, v132
	v_readfirstlane_b32 s6, v132
	s_addc_u32 s5, s5, s1
	s_add_i32 s17, s17, s7
	v_lshlrev_b32_e32 v41, 2, v1
	s_cmp_gt_u32 s6, 63
	v_cmp_eq_u32_e32 vcc, 0, v1
	v_xor_b32_e32 v40, 0x80, v41
	s_cbranch_scc1 .LBB0_869
	s_add_i32 s0, s17, 0x20870
	v_mov_b32_e32 v0, s0
	ds_read2_b32 v[38:39], v0 offset1:1
	s_lshl_b64 s[0:1], s[14:15], 2
	v_lshl_or_b32 v36, v1, 1, s29
	v_ashrrev_i32_e32 v37, 31, v36
	v_lshlrev_b64 v[36:37], 6, v[36:37]
	s_waitcnt lgkmcnt(0)
	v_readfirstlane_b32 s7, v38
	v_readfirstlane_b32 s19, v39
	s_add_u32 s20, s7, s0
	s_addc_u32 s21, s19, s1
	s_add_i32 s7, s17, 0x20868
	v_mov_b32_e32 v0, s7
	ds_read2_b32 v[42:43], v0 offset1:1
	v_lshl_add_u64 v[36:37], s[4:5], 0, v[36:37]
	v_mov_b32_e32 v38, s77
	s_waitcnt lgkmcnt(0)
	v_readfirstlane_b32 s7, v42
	v_readfirstlane_b32 s19, v43
	s_add_u32 s0, s7, s0
	s_addc_u32 s1, s19, s1
	v_mov_b32_e32 v2, s55
	s_mov_b32 s0, 0x500000
	v_add_co_u32_e64 v36, s[0:1], s0, v36
	s_nop 1
	v_addc_co_u32_e64 v37, s[0:1], 0, v37, s[0:1]
	v_mov_b32_e32 v0, v225
	v_mov_b32_e32 v153, v219
	v_mov_b32_e32 v152, v239
	v_mov_b32_e32 v151, v243
	s_nop 0
	v_add_f32_e32 v0, v38, v0
	v_min_f32_e32 v39, 0, v0
	v_mul_f32_e64 v0, |v0|, s81
	v_exp_f32_e32 v0, v0
	s_nop 0
	v_add_f32_e32 v44, 1.0, v0
	v_add_f32_e32 v42, -1.0, v44
	v_sub_f32_e32 v43, v42, v44
	v_add_f32_e32 v43, 1.0, v43
	v_sub_f32_e32 v42, v0, v42
	v_add_f32_e32 v45, v42, v43
	v_frexp_mant_f32_e32 v42, v44
	v_cmp_gt_f32_e64 s[0:1], s87, v42
	v_cvt_f64_f32_e32 v[42:43], v44
	v_frexp_exp_i32_f64_e32 v42, v[42:43]
	v_subbrev_co_u32_e64 v42, s[0:1], 0, v42, s[0:1]
	v_sub_u32_e32 v43, 0, v42
	v_ldexp_f32 v44, v44, v43
	v_ldexp_f32 v43, v45, v43
	v_add_f32_e32 v45, -1.0, v44
	v_add_f32_e32 v46, 1.0, v45
	v_sub_f32_e32 v46, v44, v46
	v_add_f32_e32 v46, v43, v46
	v_add_f32_e32 v47, v45, v46
	v_sub_f32_e32 v45, v47, v45
	v_sub_f32_e32 v45, v46, v45
	v_add_f32_e32 v46, 1.0, v44
	v_add_f32_e32 v48, -1.0, v46
	v_sub_f32_e32 v44, v44, v48
	v_add_f32_e32 v43, v43, v44
	v_add_f32_e32 v44, v46, v43
	v_sub_f32_e32 v46, v44, v46
	v_sub_f32_e32 v43, v43, v46
	v_rcp_f32_e32 v46, v44
	v_cvt_f32_i32_e32 v42, v42
	v_cmp_neq_f32_e64 s[0:1], s82, v0
	v_mul_f32_e32 v48, v47, v46
	v_mul_f32_e32 v49, v44, v48
	v_fma_f32 v50, v48, v44, -v49
	v_fmac_f32_e32 v50, v48, v43
	v_add_f32_e32 v51, v49, v50
	v_sub_f32_e32 v52, v47, v51
	v_sub_f32_e32 v47, v47, v52
	v_sub_f32_e32 v49, v51, v49
	v_sub_f32_e32 v47, v47, v51
	v_add_f32_e32 v45, v45, v47
	v_sub_f32_e32 v47, v49, v50
	v_add_f32_e32 v45, v47, v45
	v_add_f32_e32 v47, v52, v45
	v_mul_f32_e32 v49, v46, v47
	v_mul_f32_e32 v50, v44, v49
	v_fma_f32 v44, v49, v44, -v50
	v_fmac_f32_e32 v44, v49, v43
	v_sub_f32_e32 v43, v52, v47
	v_add_f32_e32 v43, v45, v43
	v_add_f32_e32 v45, v50, v44
	v_sub_f32_e32 v51, v47, v45
	v_sub_f32_e32 v47, v47, v51
	v_sub_f32_e32 v50, v45, v50
	v_sub_f32_e32 v45, v47, v45
	v_add_f32_e32 v43, v43, v45
	v_sub_f32_e32 v44, v50, v44
	v_add_f32_e32 v43, v44, v43
	v_add_f32_e32 v44, v48, v49
	v_add_f32_e32 v43, v51, v43
	v_sub_f32_e32 v45, v44, v48
	v_mul_f32_e32 v43, v46, v43
	v_sub_f32_e32 v45, v49, v45
	v_add_f32_e32 v43, v45, v43
	v_mul_f32_e32 v48, 0x3f317218, v42
	v_add_f32_e32 v45, v44, v43
	v_fma_f32 v49, v42, s80, -v48
	v_mul_f32_e32 v46, v45, v45
	v_fmac_f32_e32 v49, 0xb102e308, v42
	v_sub_f32_e32 v42, v45, v44
	v_fmamk_f32 v47, v46, 0x3e9b6dac, v216
	v_sub_f32_e32 v42, v43, v42
	v_add_f32_e32 v43, v48, v49
	v_fmaak_f32 v47, v46, v47, 0x3f2aaada
	v_sub_f32_e32 v44, v43, v48
	v_ldexp_f32 v48, v45, 1
	v_mul_f32_e32 v45, v45, v46
	v_mul_f32_e32 v45, v45, v47
	v_add_f32_e32 v46, v48, v45
	v_sub_f32_e32 v47, v46, v48
	v_ldexp_f32 v42, v42, 1
	v_sub_f32_e32 v45, v45, v47
	v_add_f32_e32 v42, v42, v45
	v_add_f32_e32 v45, v46, v42
	v_sub_f32_e32 v46, v45, v46
	v_sub_f32_e32 v42, v42, v46
	v_add_f32_e32 v46, v43, v45
	v_sub_f32_e32 v47, v46, v43
	v_sub_f32_e32 v48, v46, v47
	v_sub_f32_e32 v44, v49, v44
	v_sub_f32_e32 v43, v43, v48
	v_sub_f32_e32 v45, v45, v47
	v_add_f32_e32 v43, v45, v43
	v_add_f32_e32 v45, v44, v42
	v_sub_f32_e32 v47, v45, v44
	v_sub_f32_e32 v48, v45, v47
	v_sub_f32_e32 v44, v44, v48
	v_sub_f32_e32 v42, v42, v47
	v_add_f32_e32 v43, v45, v43
	v_add_f32_e32 v42, v42, v44
	v_add_f32_e32 v44, v46, v43
	v_sub_f32_e32 v45, v44, v46
	v_sub_f32_e32 v43, v43, v45
	v_add_f32_e32 v42, v42, v43
	v_add_f32_e32 v42, v44, v42
	v_cndmask_b32_e64 v42, v230, v42, s[0:1]
	v_cmp_ngt_f32_e64 s[0:1], -1.0, v0
	s_nop 1
	v_cndmask_b32_e64 v42, v231, v42, s[0:1]
	v_cmp_neq_f32_e64 s[0:1], -1.0, v0
; #define LAS __attribute__((address_space(3)))
; DI float log_sigmoid_f(float x) { return fminf(x, 0.f) - log1pf(__expf(-fabsf(x))); }
; DI float shup(float v, int o, int lane) { return __int_as_float(__builtin_amdgcn_ds_bpermute(((lane - o) & 63) << 2, __float_as_int(v))); }
; template <bool IS_MAX> DI void wscan2(float& x0, float& x1, int lane) {
;     x1 = IS_MAX ? fmaxf(x0, x1) : x0 + x1;
;     float s = x1;
; #pragma unroll
;     for (int o = 1; o < 64; o <<= 1) { const float y = shup(s, o, lane); if (lane >= o) s = IS_MAX ? fmaxf(s, y) : s + y; }
;     const float ex = shup(s, 1, lane);
;     if (lane > 0) { x0 = IS_MAX ? fmaxf(x0, ex) : x0 + ex; x1 = IS_MAX ? fmaxf(x1, ex) : x1 + ex; }
; }
; DI void ml_vectors(Frame& F, int l, int t0, int h, LAS float* A, LAS float* IG, LAS float* RED) {
;     (void)RED;
;     if (F.wave == 0) {
;         const int s0 = 2 * F.lane; const float* gp = (const float*)(F.ws + WS_GATES) + (size_t)(t0 + s0) * 16; const float fb = inp(F, I_FB)[l * 4 + h], ib = inp(F, I_IB)[l * 4 + h];
;         float a0 = log_sigmoid_f(gp[12 + h] + fb), a1 = log_sigmoid_f(gp[16 + 12 + h] + fb);
;         IG[s0] = gp[8 + h] + ib; IG[s0 + 1] = gp[16 + 8 + h] + ib;
;         wscan2<false>(a0, a1, F.lane);
;         A[s0] = a0; A[s0 + 1] = a1; }
;     __syncthreads();
; }
	s_nop 1
	v_cndmask_b32_e64 v42, v232, v42, s[0:1]
	v_cmp_lt_f32_e64 s[0:1], |v0|, s86
	s_nop 1
	v_cndmask_b32_e64 v0, v42, v0, s[0:1]
	v_sub_f32_e32 v42, v39, v0
	v_add_f32_e32 v0, v38, v151
	v_min_f32_e32 v43, 0, v0
	v_mul_f32_e64 v0, |v0|, s81
	v_exp_f32_e32 v0, v0
	s_nop 0
	v_add_f32_e32 v44, 1.0, v0
	v_add_f32_e32 v38, -1.0, v44
	v_sub_f32_e32 v39, v38, v44
	v_add_f32_e32 v39, 1.0, v39
	v_sub_f32_e32 v38, v0, v38
	v_add_f32_e32 v45, v38, v39
	v_frexp_mant_f32_e32 v38, v44
	v_cmp_gt_f32_e64 s[0:1], s87, v38
	v_cvt_f64_f32_e32 v[38:39], v44
	v_frexp_exp_i32_f64_e32 v38, v[38:39]
	v_subbrev_co_u32_e64 v38, s[0:1], 0, v38, s[0:1]
	v_sub_u32_e32 v39, 0, v38
	v_ldexp_f32 v44, v44, v39
	v_ldexp_f32 v39, v45, v39
	v_add_f32_e32 v45, -1.0, v44
	v_add_f32_e32 v46, 1.0, v45
	v_sub_f32_e32 v46, v44, v46
	v_add_f32_e32 v46, v39, v46
	v_add_f32_e32 v47, v45, v46
	v_sub_f32_e32 v45, v47, v45
	v_sub_f32_e32 v45, v46, v45
	v_add_f32_e32 v46, 1.0, v44
	v_add_f32_e32 v48, -1.0, v46
	v_sub_f32_e32 v44, v44, v48
	v_add_f32_e32 v39, v39, v44
	v_add_f32_e32 v44, v46, v39
	v_sub_f32_e32 v46, v44, v46
	v_sub_f32_e32 v39, v39, v46
	v_rcp_f32_e32 v46, v44
	v_cvt_f32_i32_e32 v38, v38
	v_cmp_neq_f32_e64 s[0:1], s82, v0
	v_mul_f32_e32 v48, v47, v46
	v_mul_f32_e32 v49, v44, v48
	v_fma_f32 v50, v48, v44, -v49
	v_fmac_f32_e32 v50, v48, v39
	v_add_f32_e32 v51, v49, v50
	v_sub_f32_e32 v52, v47, v51
	v_sub_f32_e32 v47, v47, v52
	v_sub_f32_e32 v49, v51, v49
	v_sub_f32_e32 v47, v47, v51
	v_add_f32_e32 v45, v45, v47
	v_sub_f32_e32 v47, v49, v50
	v_add_f32_e32 v45, v47, v45
	v_add_f32_e32 v47, v52, v45
	v_mul_f32_e32 v49, v46, v47
	v_mul_f32_e32 v50, v44, v49
	v_fma_f32 v44, v49, v44, -v50
	v_fmac_f32_e32 v44, v49, v39
	v_sub_f32_e32 v39, v52, v47
	v_add_f32_e32 v39, v45, v39
	v_add_f32_e32 v45, v50, v44
	v_sub_f32_e32 v51, v47, v45
	v_sub_f32_e32 v47, v47, v51
	v_sub_f32_e32 v50, v45, v50
	v_sub_f32_e32 v45, v47, v45
	v_add_f32_e32 v39, v39, v45
	v_sub_f32_e32 v44, v50, v44
	v_add_f32_e32 v39, v44, v39
	v_add_f32_e32 v44, v48, v49
	v_add_f32_e32 v39, v51, v39
	v_sub_f32_e32 v45, v44, v48
	v_mul_f32_e32 v39, v46, v39
	v_sub_f32_e32 v45, v49, v45
	v_add_f32_e32 v39, v45, v39
	v_mul_f32_e32 v48, 0x3f317218, v38
	v_add_f32_e32 v45, v44, v39
	v_fma_f32 v49, v38, s80, -v48
	v_mul_f32_e32 v46, v45, v45
	v_fmac_f32_e32 v49, 0xb102e308, v38
	v_sub_f32_e32 v38, v45, v44
	v_fmamk_f32 v47, v46, 0x3e9b6dac, v216
	v_sub_f32_e32 v38, v39, v38
	v_add_f32_e32 v39, v48, v49
	v_fmaak_f32 v47, v46, v47, 0x3f2aaada
	v_sub_f32_e32 v44, v39, v48
	v_ldexp_f32 v48, v45, 1
	v_mul_f32_e32 v45, v45, v46
	v_mul_f32_e32 v45, v45, v47
	v_add_f32_e32 v46, v48, v45
	v_sub_f32_e32 v47, v46, v48
	v_ldexp_f32 v38, v38, 1
	v_sub_f32_e32 v45, v45, v47
	v_add_f32_e32 v38, v38, v45
	v_add_f32_e32 v45, v46, v38
	v_sub_f32_e32 v46, v45, v46
	v_sub_f32_e32 v38, v38, v46
	v_add_f32_e32 v46, v39, v45
	v_sub_f32_e32 v47, v46, v39
	v_sub_f32_e32 v48, v46, v47
	v_sub_f32_e32 v44, v49, v44
	v_sub_f32_e32 v39, v39, v48
	v_sub_f32_e32 v45, v45, v47
	v_add_f32_e32 v39, v45, v39
	v_add_f32_e32 v45, v44, v38
	v_sub_f32_e32 v47, v45, v44
	v_sub_f32_e32 v48, v45, v47
	v_sub_f32_e32 v44, v44, v48
	v_sub_f32_e32 v38, v38, v47
	v_add_f32_e32 v39, v45, v39
	v_add_f32_e32 v38, v38, v44
	v_add_f32_e32 v44, v46, v39
	v_sub_f32_e32 v45, v44, v46
	v_sub_f32_e32 v39, v39, v45
	v_add_f32_e32 v38, v38, v39
	v_add_f32_e32 v38, v44, v38
	v_cndmask_b32_e64 v38, v230, v38, s[0:1]
	v_cmp_ngt_f32_e64 s[0:1], -1.0, v0
	v_mov_b32_e32 v39, v152
	s_nop 0
	v_cndmask_b32_e64 v38, v231, v38, s[0:1]
	v_cmp_neq_f32_e64 s[0:1], -1.0, v0
	s_nop 1
	v_cndmask_b32_e64 v38, v232, v38, s[0:1]
	v_cmp_lt_f32_e64 s[0:1], |v0|, s86
	s_nop 1
	v_cndmask_b32_e64 v0, v38, v0, s[0:1]
	v_mov_b32_e32 v38, v153
	v_sub_f32_e32 v44, v43, v0
	v_lshl_add_u32 v43, v1, 3, s17
	v_add_u32_e32 v45, 0x9b00, v43
	v_add_f32_e32 v0, v42, v44
	v_cmp_gt_u32_e64 s[0:1], 2, v1
	s_nop 0
	v_pk_add_f32 v[36:37], v[2:3], v[38:39] op_sel_hi:[0,1]
	v_add_u32_e32 v2, 0xfc, v41
	v_and_b32_e32 v2, 0xfc, v2
	ds_write2_b32 v45, v36, v37 offset1:1
	ds_bpermute_b32 v36, v2, v0
	v_add_u32_e32 v37, 0xf8, v41
	v_and_b32_e32 v37, 0xfc, v37
	s_waitcnt lgkmcnt(0)
	v_add_f32_e32 v36, v0, v36
	v_cndmask_b32_e32 v36, v36, v0, vcc
	ds_bpermute_b32 v37, v37, v36
	s_waitcnt lgkmcnt(0)
	v_add_f32_e32 v37, v36, v37
	v_cndmask_b32_e64 v36, v37, v36, s[0:1]
	v_add_u32_e32 v37, 0xf0, v41
	v_and_b32_e32 v37, 0xfc, v37
	ds_bpermute_b32 v37, v37, v36
	v_cmp_gt_u32_e64 s[0:1], 4, v1
	s_waitcnt lgkmcnt(0)
	v_add_f32_e32 v37, v36, v37
	v_cndmask_b32_e64 v36, v37, v36, s[0:1]
	v_add_u32_e32 v37, 0xe0, v41
	v_and_b32_e32 v37, 0xfc, v37
	ds_bpermute_b32 v37, v37, v36
	v_cmp_gt_u32_e64 s[0:1], 8, v1
	s_waitcnt lgkmcnt(0)
	v_add_f32_e32 v37, v36, v37
	v_cndmask_b32_e64 v36, v37, v36, s[0:1]
	v_add_u32_e32 v37, 0xc0, v41
	v_and_b32_e32 v37, 0xfc, v37
	ds_bpermute_b32 v37, v37, v36
	v_cmp_gt_u32_e64 s[0:1], 16, v1
	s_waitcnt lgkmcnt(0)
	v_add_f32_e32 v37, v36, v37
	v_cndmask_b32_e64 v36, v37, v36, s[0:1]
	ds_bpermute_b32 v37, v40, v36
	v_cmp_gt_u32_e64 s[0:1], 32, v1
	s_waitcnt lgkmcnt(0)
	v_add_f32_e32 v37, v36, v37
	v_cndmask_b32_e64 v36, v37, v36, s[0:1]
	ds_bpermute_b32 v2, v2, v36
	s_waitcnt lgkmcnt(0)
	v_add_f32_e32 v36, v42, v2
	v_add_f32_e32 v2, v0, v2
	v_cndmask_b32_e32 v36, v36, v42, vcc
	v_cndmask_b32_e32 v0, v2, v0, vcc
	v_add_u32_e32 v2, 0x9900, v43
	ds_write2_b32 v2, v36, v0 offset1:1

; #define LAS __attribute__((address_space(3)))
; DI float log_sigmoid_f(float x) { return fminf(x, 0.f) - log1pf(__expf(-fabsf(x))); }
; DI void refresh(Frame& F) { int t_ = F.tid; asm volatile("" : "+v"(t_)); F.tid = t_; F.lane = t_ & 63; F.wave = __builtin_amdgcn_readfirstlane(t_ >> 6); size_t z_ = 0; unsigned zl_ = 0; asm volatile("" : "+s"(z_), "+s"(zl_)); F.ws = F.ws + z_; F.lds = F.lds + zl_; }
; DI void ml_vectors(Frame& F, int l, int t0, int h, LAS float* A, LAS float* IG, LAS float* RED) {
;     (void)RED;
;     if (F.wave == 0) {
;         const int s0 = 2 * F.lane; const float* gp = (const float*)(F.ws + WS_GATES) + (size_t)(t0 + s0) * 16; const float fb = inp(F, I_FB)[l * 4 + h], ib = inp(F, I_IB)[l * 4 + h];
;         float a0 = log_sigmoid_f(gp[12 + h] + fb), a1 = log_sigmoid_f(gp[16 + 12 + h] + fb);
;         IG[s0] = gp[8 + h] + ib; IG[s0 + 1] = gp[16 + 8 + h] + ib;
;         wscan2<false>(a0, a1, F.lane);
;         A[s0] = a0; A[s0 + 1] = a1; }
;     __syncthreads();
; }
; DI void ml_local_unit(Frame& F, int l, int ch, int h, const MlLPre& P) {
;     refresh(F);
;     LAS bf16* VWT = (LAS bf16*)F.lds;
;     LAS bf16* KT = VWT + 80 * LP;
;     LAS float* A = (LAS float*)(F.lds + (80 + 64) * LP * 2); LAS float* IG = A + 128; LAS float* WG = IG + 128; LAS float* RED = WG + 128;
;     const int t0 = ch * CHUNK; const bf16* proj = (const bf16*)(F.ws + WS_PROJ);
;     const int s2 = (F.tid >> 3) * 2, c0 = (F.tid & 7) * 8; (void)proj;
;     const v4u rv0 = P.v0, rv1 = P.v1, rk0 = P.k0, rk1 = P.k1;
;     ml_vectors(F, l, t0, h, A, IG, RED);
.LBB0_889:
	s_or_b64 exec, exec, s[6:7]
	v_ashrrev_i32_e32 v39, 31, v38
	v_lshl_add_u64 v[0:1], s[2:3], 0, v[38:39]
	v_mov_b64_e32 v[12:13], s[4:5]
	v_mad_u64_u32 v[12:13], s[0:1], v0, s33, v[12:13]
	v_mad_i32_i24 v13, v1, s33, v13
	v_lshlrev_b32_e32 v2, 1, v40
	v_lshl_add_u64 v[0:1], v[12:13], 0, v[2:3]
	s_mov_b32 s0, 0xb101000
	v_add_co_u32_e32 v12, vcc, s0, v0
	s_mov_b32 s0, 0xb103000
	s_nop 0
	v_addc_co_u32_e32 v13, vcc, 0, v1, vcc
	v_add_co_u32_e32 v16, vcc, s0, v0
	s_mov_b32 s0, 0xb102000
	s_nop 0
	v_addc_co_u32_e32 v17, vcc, 0, v1, vcc
	v_add_co_u32_e32 v0, vcc, s0, v0
	s_barrier
	global_load_dwordx4 v[24:27], v[12:13], off offset:1920
	s_nop 0
	global_load_dwordx4 v[12:15], v[12:13], off offset:1408
	v_addc_co_u32_e32 v1, vcc, 0, v1, vcc
	global_load_dwordx4 v[32:35], v[16:17], off offset:384
	s_nop 0
	global_load_dwordx4 v[16:19], v[0:1], off offset:3968
	s_mov_b64 s[0:1], 0
	s_mov_b32 s7, s53
	s_add_u32 s2, s4, s0
	v_and_b32_e32 v1, 63, v132
	v_readfirstlane_b32 s6, v132
	s_addc_u32 s3, s5, s1
	s_add_i32 s17, s17, s7
	v_lshlrev_b32_e32 v41, 2, v1
	s_cmp_gt_u32 s6, 63
	v_cmp_eq_u32_e32 vcc, 0, v1
	v_xor_b32_e32 v40, 0x80, v41
	s_cbranch_scc1 .LBB0_891
	s_add_i32 s0, s17, 0x20870
	v_mov_b32_e32 v0, s0
	ds_read2_b32 v[38:39], v0 offset1:1
	s_lshl_b64 s[0:1], s[14:15], 2
	v_lshl_or_b32 v36, v1, 1, s29
	v_ashrrev_i32_e32 v37, 31, v36
	v_lshlrev_b64 v[36:37], 6, v[36:37]
	s_waitcnt lgkmcnt(0)
	v_readfirstlane_b32 s4, v38
	v_readfirstlane_b32 s5, v39
	s_add_u32 s4, s4, s0
	s_addc_u32 s5, s5, s1
	v_lshl_add_u64 v[36:37], s[2:3], 0, v[36:37]
	s_nop 1
	v_mov_b32_e32 v38, s78
	s_add_i32 s4, s17, 0x20868
	v_mov_b32_e32 v0, s4
	ds_read2_b32 v[42:43], v0 offset1:1
	s_waitcnt lgkmcnt(0)
	v_readfirstlane_b32 s4, v42
	v_readfirstlane_b32 s5, v43
	s_add_u32 s0, s4, s0
	s_addc_u32 s1, s5, s1
	v_mov_b32_e32 v2, s58
	s_mov_b32 s0, 0x500000
	v_add_co_u32_e64 v36, s[0:1], s0, v36
	s_nop 1
	v_addc_co_u32_e64 v37, s[0:1], 0, v37, s[0:1]
	v_mov_b32_e32 v0, v226
	v_mov_b32_e32 v153, v220
	v_mov_b32_e32 v152, v240
	v_mov_b32_e32 v151, v244
	s_nop 0
	v_add_f32_e32 v0, v38, v0
	v_min_f32_e32 v39, 0, v0
	v_mul_f32_e64 v0, |v0|, s81
	v_exp_f32_e32 v0, v0
	s_nop 0
	v_add_f32_e32 v44, 1.0, v0
	v_add_f32_e32 v42, -1.0, v44
	v_sub_f32_e32 v43, v42, v44
	v_add_f32_e32 v43, 1.0, v43
	v_sub_f32_e32 v42, v0, v42
	v_add_f32_e32 v45, v42, v43
	v_frexp_mant_f32_e32 v42, v44
	v_cmp_gt_f32_e64 s[0:1], s87, v42
	v_cvt_f64_f32_e32 v[42:43], v44
	v_frexp_exp_i32_f64_e32 v42, v[42:43]
	v_subbrev_co_u32_e64 v42, s[0:1], 0, v42, s[0:1]
	v_sub_u32_e32 v43, 0, v42
	v_ldexp_f32 v44, v44, v43
	v_ldexp_f32 v43, v45, v43
	v_add_f32_e32 v45, -1.0, v44
	v_add_f32_e32 v46, 1.0, v45
	v_sub_f32_e32 v46, v44, v46
	v_add_f32_e32 v46, v43, v46
	v_add_f32_e32 v47, v45, v46
	v_sub_f32_e32 v45, v47, v45
	v_sub_f32_e32 v45, v46, v45
	v_add_f32_e32 v46, 1.0, v44
	v_add_f32_e32 v48, -1.0, v46
	v_sub_f32_e32 v44, v44, v48
	v_add_f32_e32 v43, v43, v44
	v_add_f32_e32 v44, v46, v43
	v_sub_f32_e32 v46, v44, v46
	v_sub_f32_e32 v43, v43, v46
	v_rcp_f32_e32 v46, v44
	v_cvt_f32_i32_e32 v42, v42
	v_cmp_neq_f32_e64 s[0:1], s82, v0
	v_mul_f32_e32 v48, v47, v46
	v_mul_f32_e32 v49, v44, v48
	v_fma_f32 v50, v48, v44, -v49
	v_fmac_f32_e32 v50, v48, v43
	v_add_f32_e32 v51, v49, v50
	v_sub_f32_e32 v52, v47, v51
	v_sub_f32_e32 v47, v47, v52
	v_sub_f32_e32 v49, v51, v49
	v_sub_f32_e32 v47, v47, v51
	v_add_f32_e32 v45, v45, v47
	v_sub_f32_e32 v47, v49, v50
	v_add_f32_e32 v45, v47, v45
	v_add_f32_e32 v47, v52, v45
	v_mul_f32_e32 v49, v46, v47
	v_mul_f32_e32 v50, v44, v49
	v_fma_f32 v44, v49, v44, -v50
	v_fmac_f32_e32 v44, v49, v43
	v_sub_f32_e32 v43, v52, v47
	v_add_f32_e32 v43, v45, v43
	v_add_f32_e32 v45, v50, v44
	v_sub_f32_e32 v51, v47, v45
	v_sub_f32_e32 v47, v47, v51
	v_sub_f32_e32 v50, v45, v50
	v_sub_f32_e32 v45, v47, v45
	v_add_f32_e32 v43, v43, v45
	v_sub_f32_e32 v44, v50, v44
	v_add_f32_e32 v43, v44, v43
	v_add_f32_e32 v44, v48, v49
	v_add_f32_e32 v43, v51, v43
	v_sub_f32_e32 v45, v44, v48
	v_mul_f32_e32 v43, v46, v43
	v_sub_f32_e32 v45, v49, v45
	v_add_f32_e32 v43, v45, v43
	v_mul_f32_e32 v48, 0x3f317218, v42
	v_add_f32_e32 v45, v44, v43
	v_fma_f32 v49, v42, s80, -v48
	v_mul_f32_e32 v46, v45, v45
	v_fmac_f32_e32 v49, 0xb102e308, v42
	v_sub_f32_e32 v42, v45, v44
	v_fmamk_f32 v47, v46, 0x3e9b6dac, v216
	v_sub_f32_e32 v42, v43, v42
	v_add_f32_e32 v43, v48, v49
	v_fmaak_f32 v47, v46, v47, 0x3f2aaada
	v_sub_f32_e32 v44, v43, v48
	v_ldexp_f32 v48, v45, 1
	v_mul_f32_e32 v45, v45, v46
	v_mul_f32_e32 v45, v45, v47
	v_add_f32_e32 v46, v48, v45
	v_sub_f32_e32 v47, v46, v48
	v_ldexp_f32 v42, v42, 1
	v_sub_f32_e32 v45, v45, v47
	v_add_f32_e32 v42, v42, v45
	v_add_f32_e32 v45, v46, v42
	v_sub_f32_e32 v46, v45, v46
	v_sub_f32_e32 v42, v42, v46
	v_add_f32_e32 v46, v43, v45
	v_sub_f32_e32 v47, v46, v43
	v_sub_f32_e32 v48, v46, v47
	v_sub_f32_e32 v44, v49, v44
	v_sub_f32_e32 v43, v43, v48
	v_sub_f32_e32 v45, v45, v47
	v_add_f32_e32 v43, v45, v43
	v_add_f32_e32 v45, v44, v42
	v_sub_f32_e32 v47, v45, v44
	v_sub_f32_e32 v48, v45, v47
	v_sub_f32_e32 v44, v44, v48
	v_sub_f32_e32 v42, v42, v47
	v_add_f32_e32 v43, v45, v43
	v_add_f32_e32 v42, v42, v44
	v_add_f32_e32 v44, v46, v43
	v_sub_f32_e32 v45, v44, v46
	v_sub_f32_e32 v43, v43, v45
	v_add_f32_e32 v42, v42, v43
	v_add_f32_e32 v42, v44, v42
	v_cndmask_b32_e64 v42, v230, v42, s[0:1]
	v_cmp_ngt_f32_e64 s[0:1], -1.0, v0
	s_nop 1
	v_cndmask_b32_e64 v42, v231, v42, s[0:1]
; #define LAS __attribute__((address_space(3)))
; DI float log_sigmoid_f(float x) { return fminf(x, 0.f) - log1pf(__expf(-fabsf(x))); }
; DI float shup(float v, int o, int lane) { return __int_as_float(__builtin_amdgcn_ds_bpermute(((lane - o) & 63) << 2, __float_as_int(v))); }
; template <bool IS_MAX> DI void wscan2(float& x0, float& x1, int lane) {
;     x1 = IS_MAX ? fmaxf(x0, x1) : x0 + x1;
;     float s = x1;
; #pragma unroll
;     for (int o = 1; o < 64; o <<= 1) { const float y = shup(s, o, lane); if (lane >= o) s = IS_MAX ? fmaxf(s, y) : s + y; }
;     const float ex = shup(s, 1, lane);
;     if (lane > 0) { x0 = IS_MAX ? fmaxf(x0, ex) : x0 + ex; x1 = IS_MAX ? fmaxf(x1, ex) : x1 + ex; }
; }
; DI void ml_vectors(Frame& F, int l, int t0, int h, LAS float* A, LAS float* IG, LAS float* RED) {
;     (void)RED;
;     if (F.wave == 0) {
;         const int s0 = 2 * F.lane; const float* gp = (const float*)(F.ws + WS_GATES) + (size_t)(t0 + s0) * 16; const float fb = inp(F, I_FB)[l * 4 + h], ib = inp(F, I_IB)[l * 4 + h];
;         float a0 = log_sigmoid_f(gp[12 + h] + fb), a1 = log_sigmoid_f(gp[16 + 12 + h] + fb);
;         IG[s0] = gp[8 + h] + ib; IG[s0 + 1] = gp[16 + 8 + h] + ib;
;         wscan2<false>(a0, a1, F.lane);
;         A[s0] = a0; A[s0 + 1] = a1; }
;     __syncthreads();
; }
	v_cmp_neq_f32_e64 s[0:1], -1.0, v0
	s_nop 1
	v_cndmask_b32_e64 v42, v232, v42, s[0:1]
	v_cmp_lt_f32_e64 s[0:1], |v0|, s86
	s_nop 1
	v_cndmask_b32_e64 v0, v42, v0, s[0:1]
	v_sub_f32_e32 v42, v39, v0
	v_add_f32_e32 v0, v38, v151
	v_min_f32_e32 v43, 0, v0
	v_mul_f32_e64 v0, |v0|, s81
	v_exp_f32_e32 v0, v0
	s_nop 0
	v_add_f32_e32 v44, 1.0, v0
	v_add_f32_e32 v38, -1.0, v44
	v_sub_f32_e32 v39, v38, v44
	v_add_f32_e32 v39, 1.0, v39
	v_sub_f32_e32 v38, v0, v38
	v_add_f32_e32 v45, v38, v39
	v_frexp_mant_f32_e32 v38, v44
	v_cmp_gt_f32_e64 s[0:1], s87, v38
	v_cvt_f64_f32_e32 v[38:39], v44
	v_frexp_exp_i32_f64_e32 v38, v[38:39]
	v_subbrev_co_u32_e64 v38, s[0:1], 0, v38, s[0:1]
	v_sub_u32_e32 v39, 0, v38
	v_ldexp_f32 v44, v44, v39
	v_ldexp_f32 v39, v45, v39
	v_add_f32_e32 v45, -1.0, v44
	v_add_f32_e32 v46, 1.0, v45
	v_sub_f32_e32 v46, v44, v46
	v_add_f32_e32 v46, v39, v46
	v_add_f32_e32 v47, v45, v46
	v_sub_f32_e32 v45, v47, v45
	v_sub_f32_e32 v45, v46, v45
	v_add_f32_e32 v46, 1.0, v44
	v_add_f32_e32 v48, -1.0, v46
	v_sub_f32_e32 v44, v44, v48
	v_add_f32_e32 v39, v39, v44
	v_add_f32_e32 v44, v46, v39
	v_sub_f32_e32 v46, v44, v46
	v_sub_f32_e32 v39, v39, v46
	v_rcp_f32_e32 v46, v44
	v_cvt_f32_i32_e32 v38, v38
	v_cmp_neq_f32_e64 s[0:1], s82, v0
	v_mul_f32_e32 v48, v47, v46
	v_mul_f32_e32 v49, v44, v48
	v_fma_f32 v50, v48, v44, -v49
	v_fmac_f32_e32 v50, v48, v39
	v_add_f32_e32 v51, v49, v50
	v_sub_f32_e32 v52, v47, v51
	v_sub_f32_e32 v47, v47, v52
	v_sub_f32_e32 v49, v51, v49
	v_sub_f32_e32 v47, v47, v51
	v_add_f32_e32 v45, v45, v47
	v_sub_f32_e32 v47, v49, v50
	v_add_f32_e32 v45, v47, v45
	v_add_f32_e32 v47, v52, v45
	v_mul_f32_e32 v49, v46, v47
	v_mul_f32_e32 v50, v44, v49
	v_fma_f32 v44, v49, v44, -v50
	v_fmac_f32_e32 v44, v49, v39
	v_sub_f32_e32 v39, v52, v47
	v_add_f32_e32 v39, v45, v39
	v_add_f32_e32 v45, v50, v44
	v_sub_f32_e32 v51, v47, v45
	v_sub_f32_e32 v47, v47, v51
	v_sub_f32_e32 v50, v45, v50
	v_sub_f32_e32 v45, v47, v45
	v_add_f32_e32 v39, v39, v45
	v_sub_f32_e32 v44, v50, v44
	v_add_f32_e32 v39, v44, v39
	v_add_f32_e32 v44, v48, v49
	v_add_f32_e32 v39, v51, v39
	v_sub_f32_e32 v45, v44, v48
	v_mul_f32_e32 v39, v46, v39
	v_sub_f32_e32 v45, v49, v45
	v_add_f32_e32 v39, v45, v39
	v_mul_f32_e32 v48, 0x3f317218, v38
	v_add_f32_e32 v45, v44, v39
	v_fma_f32 v49, v38, s80, -v48
	v_mul_f32_e32 v46, v45, v45
	v_fmac_f32_e32 v49, 0xb102e308, v38
	v_sub_f32_e32 v38, v45, v44
	v_fmamk_f32 v47, v46, 0x3e9b6dac, v216
	v_sub_f32_e32 v38, v39, v38
	v_add_f32_e32 v39, v48, v49
	v_fmaak_f32 v47, v46, v47, 0x3f2aaada
	v_sub_f32_e32 v44, v39, v48
	v_ldexp_f32 v48, v45, 1
	v_mul_f32_e32 v45, v45, v46
	v_mul_f32_e32 v45, v45, v47
	v_add_f32_e32 v46, v48, v45
	v_sub_f32_e32 v47, v46, v48
	v_ldexp_f32 v38, v38, 1
	v_sub_f32_e32 v45, v45, v47
	v_add_f32_e32 v38, v38, v45
	v_add_f32_e32 v45, v46, v38
	v_sub_f32_e32 v46, v45, v46
	v_sub_f32_e32 v38, v38, v46
	v_add_f32_e32 v46, v39, v45
	v_sub_f32_e32 v47, v46, v39
	v_sub_f32_e32 v48, v46, v47
	v_sub_f32_e32 v44, v49, v44
	v_sub_f32_e32 v39, v39, v48
	v_sub_f32_e32 v45, v45, v47
	v_add_f32_e32 v39, v45, v39
	v_add_f32_e32 v45, v44, v38
	v_sub_f32_e32 v47, v45, v44
	v_sub_f32_e32 v48, v45, v47
	v_sub_f32_e32 v44, v44, v48
	v_sub_f32_e32 v38, v38, v47
	v_add_f32_e32 v39, v45, v39
	v_add_f32_e32 v38, v38, v44
	v_add_f32_e32 v44, v46, v39
	v_sub_f32_e32 v45, v44, v46
	v_sub_f32_e32 v39, v39, v45
	v_add_f32_e32 v38, v38, v39
	v_add_f32_e32 v38, v44, v38
	v_cndmask_b32_e64 v38, v230, v38, s[0:1]
	v_cmp_ngt_f32_e64 s[0:1], -1.0, v0
	v_mov_b32_e32 v39, v152
	s_nop 0
	v_cndmask_b32_e64 v38, v231, v38, s[0:1]
	v_cmp_neq_f32_e64 s[0:1], -1.0, v0
	s_nop 1
	v_cndmask_b32_e64 v38, v232, v38, s[0:1]
	v_cmp_lt_f32_e64 s[0:1], |v0|, s86
	s_nop 1
	v_cndmask_b32_e64 v0, v38, v0, s[0:1]
	v_mov_b32_e32 v38, v153
	v_sub_f32_e32 v44, v43, v0
	v_lshl_add_u32 v43, v1, 3, s17
	v_add_u32_e32 v45, 0x9b00, v43
	v_add_f32_e32 v0, v42, v44
	v_cmp_gt_u32_e64 s[0:1], 2, v1
	s_nop 0
	v_pk_add_f32 v[36:37], v[2:3], v[38:39] op_sel_hi:[0,1]
	v_add_u32_e32 v2, 0xfc, v41
	v_and_b32_e32 v2, 0xfc, v2
	ds_write2_b32 v45, v36, v37 offset1:1
	ds_bpermute_b32 v36, v2, v0
	v_add_u32_e32 v37, 0xf8, v41
	v_and_b32_e32 v37, 0xfc, v37
	s_waitcnt lgkmcnt(0)
	v_add_f32_e32 v36, v0, v36
	v_cndmask_b32_e32 v36, v36, v0, vcc
	ds_bpermute_b32 v37, v37, v36
	s_waitcnt lgkmcnt(0)
	v_add_f32_e32 v37, v36, v37
	v_cndmask_b32_e64 v36, v37, v36, s[0:1]
	v_add_u32_e32 v37, 0xf0, v41
	v_and_b32_e32 v37, 0xfc, v37
	ds_bpermute_b32 v37, v37, v36
	v_cmp_gt_u32_e64 s[0:1], 4, v1
	s_waitcnt lgkmcnt(0)
	v_add_f32_e32 v37, v36, v37
	v_cndmask_b32_e64 v36, v37, v36, s[0:1]
	v_add_u32_e32 v37, 0xe0, v41
	v_and_b32_e32 v37, 0xfc, v37
	ds_bpermute_b32 v37, v37, v36
	v_cmp_gt_u32_e64 s[0:1], 8, v1
	s_waitcnt lgkmcnt(0)
	v_add_f32_e32 v37, v36, v37
	v_cndmask_b32_e64 v36, v37, v36, s[0:1]
	v_add_u32_e32 v37, 0xc0, v41
	v_and_b32_e32 v37, 0xfc, v37
	ds_bpermute_b32 v37, v37, v36
	v_cmp_gt_u32_e64 s[0:1], 16, v1
	s_waitcnt lgkmcnt(0)
	v_add_f32_e32 v37, v36, v37
	v_cndmask_b32_e64 v36, v37, v36, s[0:1]
	ds_bpermute_b32 v37, v40, v36
	v_cmp_gt_u32_e64 s[0:1], 32, v1
	s_waitcnt lgkmcnt(0)
	v_add_f32_e32 v37, v36, v37
	v_cndmask_b32_e64 v36, v37, v36, s[0:1]
	ds_bpermute_b32 v2, v2, v36
	s_waitcnt lgkmcnt(0)
	v_add_f32_e32 v36, v42, v2
	v_add_f32_e32 v2, v0, v2
	v_cndmask_b32_e32 v36, v36, v42, vcc
	v_cndmask_b32_e32 v0, v2, v0, vcc
	v_add_u32_e32 v2, 0x9900, v43
	ds_write2_b32 v2, v36, v0 offset1:1

; #define LAS __attribute__((address_space(3)))
; DI float log_sigmoid_f(float x) { return fminf(x, 0.f) - log1pf(__expf(-fabsf(x))); }
; DI void refresh(Frame& F) { int t_ = F.tid; asm volatile("" : "+v"(t_)); F.tid = t_; F.lane = t_ & 63; F.wave = __builtin_amdgcn_readfirstlane(t_ >> 6); size_t z_ = 0; unsigned zl_ = 0; asm volatile("" : "+s"(z_), "+s"(zl_)); F.ws = F.ws + z_; F.lds = F.lds + zl_; }
; DI void ml_vectors(Frame& F, int l, int t0, int h, LAS float* A, LAS float* IG, LAS float* RED) {
;     (void)RED;
;     if (F.wave == 0) {
;         const int s0 = 2 * F.lane; const float* gp = (const float*)(F.ws + WS_GATES) + (size_t)(t0 + s0) * 16; const float fb = inp(F, I_FB)[l * 4 + h], ib = inp(F, I_IB)[l * 4 + h];
;         float a0 = log_sigmoid_f(gp[12 + h] + fb), a1 = log_sigmoid_f(gp[16 + 12 + h] + fb);
;         IG[s0] = gp[8 + h] + ib; IG[s0 + 1] = gp[16 + 8 + h] + ib;
;         wscan2<false>(a0, a1, F.lane);
;         A[s0] = a0; A[s0 + 1] = a1; }
;     __syncthreads();
; }
; DI void ml_local_unit(Frame& F, int l, int ch, int h, const MlLPre& P) {
;     refresh(F);
;     LAS bf16* VWT = (LAS bf16*)F.lds;
;     LAS bf16* KT = VWT + 80 * LP;
;     LAS float* A = (LAS float*)(F.lds + (80 + 64) * LP * 2); LAS float* IG = A + 128; LAS float* WG = IG + 128; LAS float* RED = WG + 128;
;     const int t0 = ch * CHUNK; const bf16* proj = (const bf16*)(F.ws + WS_PROJ);
;     const int s2 = (F.tid >> 3) * 2, c0 = (F.tid & 7) * 8; (void)proj;
;     const v4u rv0 = P.v0, rv1 = P.v1, rk0 = P.k0, rk1 = P.k1;
;     ml_vectors(F, l, t0, h, A, IG, RED);
.LBB0_911:
	s_or_b64 exec, exec, s[4:5]
	s_mov_b64 s[0:1], 0
	s_mov_b32 s5, s53
	s_barrier
	s_add_u32 s20, s2, s0
	v_and_b32_e32 v1, 63, v132
	v_readfirstlane_b32 s4, v132
	s_addc_u32 s21, s3, s1
	s_add_i32 s17, s17, s5
	v_lshlrev_b32_e32 v9, 2, v1
	s_cmp_gt_u32 s4, 63
	v_cmp_eq_u32_e32 vcc, 0, v1
	v_xor_b32_e32 v8, 0x80, v9
	s_cbranch_scc1 .LBB0_913
	s_add_i32 s0, s17, 0x20870
	v_mov_b32_e32 v0, s0
	ds_read2_b32 v[6:7], v0 offset1:1
	s_lshl_b64 s[0:1], s[14:15], 2
	v_lshl_or_b32 v4, v1, 1, s29
	v_ashrrev_i32_e32 v5, 31, v4
	v_lshlrev_b64 v[4:5], 6, v[4:5]
	s_waitcnt lgkmcnt(0)
	v_readfirstlane_b32 s2, v6
	v_readfirstlane_b32 s3, v7
	s_add_u32 s2, s2, s0
	s_addc_u32 s3, s3, s1
	v_lshl_add_u64 v[4:5], s[20:21], 0, v[4:5]
	s_nop 1
	v_mov_b32_e32 v6, s79
	s_add_i32 s2, s17, 0x20868
	v_mov_b32_e32 v0, s2
	ds_read2_b32 v[10:11], v0 offset1:1
	s_waitcnt lgkmcnt(0)
	v_readfirstlane_b32 s2, v10
	v_readfirstlane_b32 s3, v11
	s_add_u32 s0, s2, s0
	s_addc_u32 s1, s3, s1
	v_mov_b32_e32 v2, s59
	s_mov_b32 s0, 0x500000
	v_add_co_u32_e64 v4, s[0:1], s0, v4
	s_nop 1
	v_addc_co_u32_e64 v5, s[0:1], 0, v5, s[0:1]
	v_mov_b32_e32 v0, v227
	v_mov_b32_e32 v153, v221
	v_mov_b32_e32 v152, v241
	v_mov_b32_e32 v151, v245
	s_nop 0
	v_add_f32_e32 v0, v6, v0
	v_min_f32_e32 v7, 0, v0
	v_mul_f32_e64 v0, |v0|, s81
	v_exp_f32_e32 v0, v0
	s_nop 0
	v_add_f32_e32 v20, 1.0, v0
	v_add_f32_e32 v10, -1.0, v20
	v_sub_f32_e32 v11, v10, v20
	v_add_f32_e32 v11, 1.0, v11
	v_sub_f32_e32 v10, v0, v10
	v_add_f32_e32 v21, v10, v11
	v_frexp_mant_f32_e32 v10, v20
	v_cmp_gt_f32_e64 s[0:1], s87, v10
	v_cvt_f64_f32_e32 v[10:11], v20
	v_frexp_exp_i32_f64_e32 v10, v[10:11]
	v_subbrev_co_u32_e64 v10, s[0:1], 0, v10, s[0:1]
	v_sub_u32_e32 v11, 0, v10
	v_ldexp_f32 v20, v20, v11
	v_ldexp_f32 v11, v21, v11
	v_add_f32_e32 v21, -1.0, v20
	v_add_f32_e32 v22, 1.0, v21
	v_sub_f32_e32 v22, v20, v22
	v_add_f32_e32 v22, v11, v22
	v_add_f32_e32 v23, v21, v22
	v_sub_f32_e32 v21, v23, v21
	v_sub_f32_e32 v21, v22, v21
	v_add_f32_e32 v22, 1.0, v20
	v_add_f32_e32 v28, -1.0, v22
	v_sub_f32_e32 v20, v20, v28
	v_add_f32_e32 v11, v11, v20
	v_add_f32_e32 v20, v22, v11
	v_sub_f32_e32 v22, v20, v22
	v_sub_f32_e32 v11, v11, v22
	v_rcp_f32_e32 v22, v20
	v_cvt_f32_i32_e32 v10, v10
	v_cmp_neq_f32_e64 s[0:1], s82, v0
	v_mul_f32_e32 v28, v23, v22
	v_mul_f32_e32 v29, v20, v28
	v_fma_f32 v30, v28, v20, -v29
	v_fmac_f32_e32 v30, v28, v11
	v_add_f32_e32 v31, v29, v30
	v_sub_f32_e32 v36, v23, v31
	v_sub_f32_e32 v23, v23, v36
	v_sub_f32_e32 v29, v31, v29
	v_sub_f32_e32 v23, v23, v31
	v_add_f32_e32 v21, v21, v23
	v_sub_f32_e32 v23, v29, v30
	v_add_f32_e32 v21, v23, v21
	v_add_f32_e32 v23, v36, v21
	v_mul_f32_e32 v29, v22, v23
	v_mul_f32_e32 v30, v20, v29
	v_fma_f32 v20, v29, v20, -v30
	v_fmac_f32_e32 v20, v29, v11
	v_sub_f32_e32 v11, v36, v23
	v_add_f32_e32 v11, v21, v11
	v_add_f32_e32 v21, v30, v20
	v_sub_f32_e32 v31, v23, v21
	v_sub_f32_e32 v23, v23, v31
	v_sub_f32_e32 v30, v21, v30
	v_sub_f32_e32 v21, v23, v21
	v_add_f32_e32 v11, v11, v21
	v_sub_f32_e32 v20, v30, v20
	v_add_f32_e32 v11, v20, v11
	v_add_f32_e32 v20, v28, v29
	v_add_f32_e32 v11, v31, v11
	v_sub_f32_e32 v21, v20, v28
	v_mul_f32_e32 v11, v22, v11
	v_sub_f32_e32 v21, v29, v21
	v_add_f32_e32 v11, v21, v11
	v_mul_f32_e32 v28, 0x3f317218, v10
	v_add_f32_e32 v21, v20, v11
	v_fma_f32 v29, v10, s80, -v28
	v_mul_f32_e32 v22, v21, v21
	v_fmac_f32_e32 v29, 0xb102e308, v10
	v_sub_f32_e32 v10, v21, v20
	v_fmamk_f32 v23, v22, 0x3e9b6dac, v216
	v_sub_f32_e32 v10, v11, v10
	v_add_f32_e32 v11, v28, v29
	v_fmaak_f32 v23, v22, v23, 0x3f2aaada
	v_sub_f32_e32 v20, v11, v28
	v_ldexp_f32 v28, v21, 1
	v_mul_f32_e32 v21, v21, v22
	v_mul_f32_e32 v21, v21, v23
	v_add_f32_e32 v22, v28, v21
	v_sub_f32_e32 v23, v22, v28
	v_ldexp_f32 v10, v10, 1
	v_sub_f32_e32 v21, v21, v23
	v_add_f32_e32 v10, v10, v21
	v_add_f32_e32 v21, v22, v10
	v_sub_f32_e32 v22, v21, v22
	v_sub_f32_e32 v10, v10, v22
	v_add_f32_e32 v22, v11, v21
	v_sub_f32_e32 v23, v22, v11
	v_sub_f32_e32 v28, v22, v23
	v_sub_f32_e32 v20, v29, v20
	v_sub_f32_e32 v11, v11, v28
	v_sub_f32_e32 v21, v21, v23
	v_add_f32_e32 v11, v21, v11
	v_add_f32_e32 v21, v20, v10
	v_sub_f32_e32 v23, v21, v20
	v_sub_f32_e32 v28, v21, v23
	v_sub_f32_e32 v20, v20, v28
	v_sub_f32_e32 v10, v10, v23
	v_add_f32_e32 v11, v21, v11
	v_add_f32_e32 v10, v10, v20
	v_add_f32_e32 v20, v22, v11
	v_sub_f32_e32 v21, v20, v22
	v_sub_f32_e32 v11, v11, v21
	v_add_f32_e32 v10, v10, v11
	v_add_f32_e32 v10, v20, v10
	v_cndmask_b32_e64 v10, v230, v10, s[0:1]
	v_cmp_ngt_f32_e64 s[0:1], -1.0, v0
	s_nop 1
	v_cndmask_b32_e64 v10, v231, v10, s[0:1]
	v_cmp_neq_f32_e64 s[0:1], -1.0, v0
	s_nop 1
	v_cndmask_b32_e64 v10, v232, v10, s[0:1]
	v_cmp_lt_f32_e64 s[0:1], |v0|, s86
	s_nop 1
	v_cndmask_b32_e64 v0, v10, v0, s[0:1]
	v_sub_f32_e32 v10, v7, v0
	v_add_f32_e32 v0, v6, v151
	v_min_f32_e32 v11, 0, v0
	v_mul_f32_e64 v0, |v0|, s81
	v_exp_f32_e32 v0, v0
	s_nop 0
	v_add_f32_e32 v20, 1.0, v0
; #define LAS __attribute__((address_space(3)))
; DI float log_sigmoid_f(float x) { return fminf(x, 0.f) - log1pf(__expf(-fabsf(x))); }
; DI float shup(float v, int o, int lane) { return __int_as_float(__builtin_amdgcn_ds_bpermute(((lane - o) & 63) << 2, __float_as_int(v))); }
; template <bool IS_MAX> DI void wscan2(float& x0, float& x1, int lane) {
;     x1 = IS_MAX ? fmaxf(x0, x1) : x0 + x1;
;     float s = x1;
; #pragma unroll
;     for (int o = 1; o < 64; o <<= 1) { const float y = shup(s, o, lane); if (lane >= o) s = IS_MAX ? fmaxf(s, y) : s + y; }
;     const float ex = shup(s, 1, lane);
;     if (lane > 0) { x0 = IS_MAX ? fmaxf(x0, ex) : x0 + ex; x1 = IS_MAX ? fmaxf(x1, ex) : x1 + ex; }
; }
; DI void ml_vectors(Frame& F, int l, int t0, int h, LAS float* A, LAS float* IG, LAS float* RED) {
;     (void)RED;
;     if (F.wave == 0) {
;         const int s0 = 2 * F.lane; const float* gp = (const float*)(F.ws + WS_GATES) + (size_t)(t0 + s0) * 16; const float fb = inp(F, I_FB)[l * 4 + h], ib = inp(F, I_IB)[l * 4 + h];
;         float a0 = log_sigmoid_f(gp[12 + h] + fb), a1 = log_sigmoid_f(gp[16 + 12 + h] + fb);
;         IG[s0] = gp[8 + h] + ib; IG[s0 + 1] = gp[16 + 8 + h] + ib;
;         wscan2<false>(a0, a1, F.lane);
;         A[s0] = a0; A[s0 + 1] = a1; }
;     __syncthreads();
; }
	v_add_f32_e32 v6, -1.0, v20
	v_sub_f32_e32 v7, v6, v20
	v_add_f32_e32 v7, 1.0, v7
	v_sub_f32_e32 v6, v0, v6
	v_add_f32_e32 v21, v6, v7
	v_frexp_mant_f32_e32 v6, v20
	v_cmp_gt_f32_e64 s[0:1], s87, v6
	v_cvt_f64_f32_e32 v[6:7], v20
	v_frexp_exp_i32_f64_e32 v6, v[6:7]
	v_subbrev_co_u32_e64 v6, s[0:1], 0, v6, s[0:1]
	v_sub_u32_e32 v7, 0, v6
	v_ldexp_f32 v20, v20, v7
	v_ldexp_f32 v7, v21, v7
	v_add_f32_e32 v21, -1.0, v20
	v_add_f32_e32 v22, 1.0, v21
	v_sub_f32_e32 v22, v20, v22
	v_add_f32_e32 v22, v7, v22
	v_add_f32_e32 v23, v21, v22
	v_sub_f32_e32 v21, v23, v21
	v_sub_f32_e32 v21, v22, v21
	v_add_f32_e32 v22, 1.0, v20
	v_add_f32_e32 v28, -1.0, v22
	v_sub_f32_e32 v20, v20, v28
	v_add_f32_e32 v7, v7, v20
	v_add_f32_e32 v20, v22, v7
	v_sub_f32_e32 v22, v20, v22
	v_sub_f32_e32 v7, v7, v22
	v_rcp_f32_e32 v22, v20
	v_cvt_f32_i32_e32 v6, v6
	v_cmp_neq_f32_e64 s[0:1], s82, v0
	v_mul_f32_e32 v28, v23, v22
	v_mul_f32_e32 v29, v20, v28
	v_fma_f32 v30, v28, v20, -v29
	v_fmac_f32_e32 v30, v28, v7
	v_add_f32_e32 v31, v29, v30
	v_sub_f32_e32 v36, v23, v31
	v_sub_f32_e32 v23, v23, v36
	v_sub_f32_e32 v29, v31, v29
	v_sub_f32_e32 v23, v23, v31
	v_add_f32_e32 v21, v21, v23
	v_sub_f32_e32 v23, v29, v30
	v_add_f32_e32 v21, v23, v21
	v_add_f32_e32 v23, v36, v21
	v_mul_f32_e32 v29, v22, v23
	v_mul_f32_e32 v30, v20, v29
	v_fma_f32 v20, v29, v20, -v30
	v_fmac_f32_e32 v20, v29, v7
	v_sub_f32_e32 v7, v36, v23
	v_add_f32_e32 v7, v21, v7
	v_add_f32_e32 v21, v30, v20
	v_sub_f32_e32 v31, v23, v21
	v_sub_f32_e32 v23, v23, v31
	v_sub_f32_e32 v30, v21, v30
	v_sub_f32_e32 v21, v23, v21
	v_add_f32_e32 v7, v7, v21
	v_sub_f32_e32 v20, v30, v20
	v_add_f32_e32 v7, v20, v7
	v_add_f32_e32 v20, v28, v29
	v_add_f32_e32 v7, v31, v7
	v_sub_f32_e32 v21, v20, v28
	v_mul_f32_e32 v7, v22, v7
	v_sub_f32_e32 v21, v29, v21
	v_add_f32_e32 v7, v21, v7
	v_mul_f32_e32 v28, 0x3f317218, v6
	v_add_f32_e32 v21, v20, v7
	v_fma_f32 v29, v6, s80, -v28
	v_mul_f32_e32 v22, v21, v21
	v_fmac_f32_e32 v29, 0xb102e308, v6
	v_sub_f32_e32 v6, v21, v20
	v_fmamk_f32 v23, v22, 0x3e9b6dac, v216
	v_sub_f32_e32 v6, v7, v6
	v_add_f32_e32 v7, v28, v29
	v_fmaak_f32 v23, v22, v23, 0x3f2aaada
	v_sub_f32_e32 v20, v7, v28
	v_ldexp_f32 v28, v21, 1
	v_mul_f32_e32 v21, v21, v22
	v_mul_f32_e32 v21, v21, v23
	v_add_f32_e32 v22, v28, v21
	v_sub_f32_e32 v23, v22, v28
	v_ldexp_f32 v6, v6, 1
	v_sub_f32_e32 v21, v21, v23
	v_add_f32_e32 v6, v6, v21
	v_add_f32_e32 v21, v22, v6
	v_sub_f32_e32 v22, v21, v22
	v_sub_f32_e32 v6, v6, v22
	v_add_f32_e32 v22, v7, v21
	v_sub_f32_e32 v23, v22, v7
	v_sub_f32_e32 v28, v22, v23
	v_sub_f32_e32 v20, v29, v20
	v_sub_f32_e32 v7, v7, v28
	v_sub_f32_e32 v21, v21, v23
	v_add_f32_e32 v7, v21, v7
	v_add_f32_e32 v21, v20, v6
	v_sub_f32_e32 v23, v21, v20
	v_sub_f32_e32 v28, v21, v23
	v_sub_f32_e32 v20, v20, v28
	v_sub_f32_e32 v6, v6, v23
	v_add_f32_e32 v7, v21, v7
	v_add_f32_e32 v6, v6, v20
	v_add_f32_e32 v20, v22, v7
	v_sub_f32_e32 v21, v20, v22
	v_sub_f32_e32 v7, v7, v21
	v_add_f32_e32 v6, v6, v7
	v_add_f32_e32 v6, v20, v6
	v_cndmask_b32_e64 v6, v230, v6, s[0:1]
	v_cmp_ngt_f32_e64 s[0:1], -1.0, v0
	v_mov_b32_e32 v7, v152
	s_nop 0
	v_cndmask_b32_e64 v6, v231, v6, s[0:1]
	v_cmp_neq_f32_e64 s[0:1], -1.0, v0
	s_nop 1
	v_cndmask_b32_e64 v6, v232, v6, s[0:1]
	v_cmp_lt_f32_e64 s[0:1], |v0|, s86
	s_nop 1
	v_cndmask_b32_e64 v0, v6, v0, s[0:1]
	v_mov_b32_e32 v6, v153
	v_sub_f32_e32 v20, v11, v0
	v_lshl_add_u32 v11, v1, 3, s17
	v_add_u32_e32 v21, 0x9b00, v11
	v_add_f32_e32 v0, v10, v20
	v_cmp_gt_u32_e64 s[0:1], 2, v1
	s_nop 0
	v_pk_add_f32 v[4:5], v[2:3], v[6:7] op_sel_hi:[0,1]
	v_add_u32_e32 v2, 0xfc, v9
	v_and_b32_e32 v2, 0xfc, v2
	ds_write2_b32 v21, v4, v5 offset1:1
	ds_bpermute_b32 v4, v2, v0
	v_add_u32_e32 v5, 0xf8, v9
	v_and_b32_e32 v5, 0xfc, v5
	s_waitcnt lgkmcnt(0)
	v_add_f32_e32 v4, v0, v4
	v_cndmask_b32_e32 v4, v4, v0, vcc
	ds_bpermute_b32 v5, v5, v4
	s_waitcnt lgkmcnt(0)
	v_add_f32_e32 v5, v4, v5
	v_cndmask_b32_e64 v4, v5, v4, s[0:1]
	v_add_u32_e32 v5, 0xf0, v9
	v_and_b32_e32 v5, 0xfc, v5
	ds_bpermute_b32 v5, v5, v4
	v_cmp_gt_u32_e64 s[0:1], 4, v1
	s_waitcnt lgkmcnt(0)
	v_add_f32_e32 v5, v4, v5
	v_cndmask_b32_e64 v4, v5, v4, s[0:1]
	v_add_u32_e32 v5, 0xe0, v9
	v_and_b32_e32 v5, 0xfc, v5
	ds_bpermute_b32 v5, v5, v4
	v_cmp_gt_u32_e64 s[0:1], 8, v1
	s_waitcnt lgkmcnt(0)
	v_add_f32_e32 v5, v4, v5
	v_cndmask_b32_e64 v4, v5, v4, s[0:1]
	v_add_u32_e32 v5, 0xc0, v9
	v_and_b32_e32 v5, 0xfc, v5
	ds_bpermute_b32 v5, v5, v4
	v_cmp_gt_u32_e64 s[0:1], 16, v1
	s_waitcnt lgkmcnt(0)
	v_add_f32_e32 v5, v4, v5
	v_cndmask_b32_e64 v4, v5, v4, s[0:1]
	ds_bpermute_b32 v5, v8, v4
	v_cmp_gt_u32_e64 s[0:1], 32, v1
	s_waitcnt lgkmcnt(0)
	v_add_f32_e32 v5, v4, v5
	v_cndmask_b32_e64 v4, v5, v4, s[0:1]
	ds_bpermute_b32 v2, v2, v4
	s_waitcnt lgkmcnt(0)
	v_add_f32_e32 v4, v10, v2
	v_add_f32_e32 v2, v0, v2
	v_cndmask_b32_e32 v4, v4, v10, vcc
	v_cndmask_b32_e32 v0, v2, v0, vcc
	v_add_u32_e32 v2, 0x9900, v11
	ds_write2_b32 v2, v4, v0 offset1:1
